# v33 + ssd_out: first state-fragment group fetched at start of lf section; epilogue z loads of first l-tile issued together (both variants)
# speedup vs baseline: 1.0086x; 1.0023x over previous
.LBB0_1238:
	s_and_b32 s21, s54, 7
	s_lshl_b32 s0, s21, 3
	s_add_i32 s22, s0, s34
	s_lshl_b32 s14, s22, 6
	s_ashr_i32 s20, s54, 3
	s_ashr_i32 s15, s14, 31
	s_lshl_b32 s55, s20, 6
	s_lshl_b64 s[16:17], s[14:15], 1
	s_waitcnt vmcnt(8)
	v_or_b32_e32 v30, s55, v167
	v_lshl_add_u64 v[28:29], v[158:159], 0, s[16:17]
	v_mad_i64_i32 v[0:1], s[0:1], v30, s77, v[28:29]
	v_or_b32_e32 v4, 8, v30
	global_load_dwordx4 v[0:3], v[0:1], off
	v_mad_i64_i32 v[4:5], s[0:1], v4, s77, v[28:29]
	v_or_b32_e32 v8, 16, v30
	global_load_dwordx4 v[4:7], v[4:5], off
	v_mad_i64_i32 v[8:9], s[0:1], v8, s77, v[28:29]
	v_or_b32_e32 v12, 24, v30
	global_load_dwordx4 v[8:11], v[8:9], off
	v_mad_i64_i32 v[12:13], s[0:1], v12, s77, v[28:29]
	v_or_b32_e32 v16, 32, v30
	global_load_dwordx4 v[12:15], v[12:13], off
	v_mad_i64_i32 v[16:17], s[0:1], v16, s77, v[28:29]
	v_or_b32_e32 v20, 40, v30
	global_load_dwordx4 v[16:19], v[16:17], off
	v_mad_i64_i32 v[20:21], s[0:1], v20, s77, v[28:29]
	v_or_b32_e32 v24, 48, v30
	global_load_dwordx4 v[20:23], v[20:21], off
	v_mad_i64_i32 v[24:25], s[0:1], v24, s77, v[28:29]
	v_or_b32_e32 v30, 56, v30
	global_load_dwordx4 v[24:27], v[24:25], off
	v_mad_i64_i32 v[28:29], s[0:1], v30, s77, v[28:29]
	global_load_dwordx4 v[28:31], v[28:29], off
	s_lshl_b32 s0, s20, 6
	s_add_i32 s0, s0, s22
	s_lshl_b32 s0, s0, 9
	v_lshl_add_u32 v198, v161, 3, s0
	v_mov_b32_e32 v199, 0
	v_lshl_add_u64 v[198:199], s[24:25], 0, v[198:199]
	s_mov_b64 s[0:1], 0x400000
	s_nop 0
	v_lshl_add_u64 v[198:199], v[198:199], 0, s[0:1]
	global_load_dwordx2 v[198:199], v[198:199], off
	s_ashr_i32 s23, s22, 31
	s_lshl_b64 s[18:19], s[22:23], 2
	s_add_u32 s0, s26, s18
	s_addc_u32 s1, s27, s19
	v_or_b32_e32 v174, s55, v166
	v_lshlrev_b32_e32 v32, 1, v160
	s_movk_i32 s56, 0x2000
	v_mov_b32_e32 v173, v33
	s_waitcnt vmcnt(8)
	ds_write_b128 v213, v[0:3]
	s_waitcnt vmcnt(7)
	ds_write_b128 v213, v[4:7] offset:1280
	s_waitcnt vmcnt(6)
	ds_write_b128 v213, v[8:11] offset:2560
	s_waitcnt vmcnt(5)
	ds_write_b128 v213, v[12:15] offset:3840
	s_waitcnt vmcnt(4)
	ds_write_b128 v213, v[16:19] offset:5120
	s_waitcnt vmcnt(3)
	ds_write_b128 v213, v[20:23] offset:6400
	s_waitcnt vmcnt(2)
	ds_write_b128 v213, v[24:27] offset:7680
	s_waitcnt vmcnt(1)
	ds_write_b128 v213, v[28:31] offset:8960
	s_lshl_b32 s86, s21, 8
	s_ashr_i32 s21, s20, 31
	s_waitcnt vmcnt(0)
	ds_write_b32 v190, v198
	ds_write_b32 v191, v199
	v_mov_b64_e32 v[0:1], s[8:9]
	v_mad_i64_i32 v[0:1], s[0:1], v174, s77, v[0:1]
	v_lshl_add_u64 v[0:1], v[0:1], 0, s[86:87]
	v_lshl_add_u64 v[8:9], v[0:1], 0, v[32:33]
	s_mov_b64 s[0:1], 0x2800
	v_lshl_add_u64 v[74:75], v[8:9], 0, s[0:1]
	v_add_co_u32_e64 v0, s[0:1], s56, v8
	s_movk_i32 s77, 0x3000
	s_nop 0
	v_addc_co_u32_e64 v1, s[0:1], 0, v9, s[0:1]
	s_mov_b32 s0, 0x32000
	s_nop 0
	v_add_co_u32_e64 v30, s[0:1], s0, v8
	global_load_dwordx4 v[4:7], v[0:1], off offset:2048
	s_nop 0
	global_load_dwordx4 v[0:3], v[74:75], off offset:64
	global_load_dwordx4 v[70:73], v[74:75], off offset:128
	global_load_dwordx4 v[66:69], v[74:75], off offset:192
	v_addc_co_u32_e64 v31, s[0:1], 0, v9, s[0:1]
	s_mov_b32 s0, 0x62000
	s_nop 0
	v_add_co_u32_e64 v88, s[0:1], s0, v8
	global_load_dwordx4 v[62:65], v[30:31], off offset:2048
	global_load_dwordx4 v[58:61], v[30:31], off offset:2112
	global_load_dwordx4 v[54:57], v[30:31], off offset:2176
	global_load_dwordx4 v[50:53], v[30:31], off offset:2240
	v_addc_co_u32_e64 v89, s[0:1], 0, v9, s[0:1]
	s_mov_b32 s0, 0x92000
	s_nop 0
	v_add_co_u32_e64 v86, s[0:1], s0, v8
	global_load_dwordx4 v[46:49], v[88:89], off offset:2048
	global_load_dwordx4 v[42:45], v[88:89], off offset:2112
	global_load_dwordx4 v[38:41], v[88:89], off offset:2176
	global_load_dwordx4 v[24:27], v[88:89], off offset:2240
	v_addc_co_u32_e64 v87, s[0:1], 0, v9, s[0:1]
	global_load_dwordx4 v[20:23], v[86:87], off offset:2048
	global_load_dwordx4 v[16:19], v[86:87], off offset:2112
	global_load_dwordx4 v[8:11], v[86:87], off offset:2176
	global_load_dwordx4 v[12:15], v[86:87], off offset:2240
	s_waitcnt lgkmcnt(0)
	ds_read2_b32 v[102:103], v192 offset1:16
	ds_read2_b32 v[28:29], v192 offset0:32 offset1:48
	global_load_dwordx4 v[82:85], v[74:75], off offset:-2048
	global_load_dwordx4 v[92:95], v[74:75], off offset:-1984
	global_load_dwordx4 v[96:99], v[74:75], off offset:-1920
	global_load_dwordx4 v[104:107], v[74:75], off offset:-1856
	s_lshl_b32 s0, s20, 12
	s_lshl_b32 s1, s22, 6
	s_add_i32 s0, s0, s1
	v_or_b32_e32 v200, s0, v166
	v_mov_b32_e32 v201, 0
	v_lshlrev_b64 v[200:201], 8, v[200:201]
	v_lshl_add_u64 v[200:201], v[164:165], 0, v[200:201]
	global_load_dwordx4 v[144:147], v[200:201], off
	global_load_dwordx4 v[148:151], v[200:201], off offset:64
	global_load_dwordx4 v[152:155], v[200:201], off offset:128
	global_load_dwordx4 v[138:141], v[200:201], off offset:192
	s_waitcnt vmcnt(7)
	v_mfma_f32_16x16x32_bf16 v[74:77], v[82:85], v[4:7], 0
	ds_read_b64 v[100:101], v193
	ds_read_b32 v32, v195
	ds_read_b32 v90, v196
	ds_read_b32 v118, v197
	ds_read_b32 v91, v208
	s_mov_b32 s0, 0x5040100
	s_waitcnt vmcnt(6)
	v_mfma_f32_16x16x32_bf16 v[74:77], v[92:95], v[0:3], v[74:77]
	s_waitcnt vmcnt(5)
	v_mfma_f32_16x16x32_bf16 v[74:77], v[96:99], v[70:73], v[74:77]
	v_mfma_f32_16x16x32_bf16 v[108:111], v[82:85], v[62:65], 0
	s_waitcnt vmcnt(4)
	v_mfma_f32_16x16x32_bf16 v[78:81], v[104:107], v[66:69], v[74:77]
	s_waitcnt lgkmcnt(4)
	s_nop 3
	v_sub_f32_e32 v76, v103, v100
	v_min_f32_e32 v76, 0, v76
	v_mfma_f32_16x16x32_bf16 v[108:111], v[92:95], v[58:61], v[108:111]
	v_mul_f32_e32 v76, 0x3fb8aa3b, v76
	v_exp_f32_e32 v114, v76
	v_sub_f32_e32 v76, v103, v101
	v_min_f32_e32 v76, 0, v76
	v_mul_f32_e32 v76, 0x3fb8aa3b, v76
	v_mfma_f32_16x16x32_bf16 v[108:111], v[96:99], v[54:57], v[108:111]
	v_exp_f32_e32 v115, v76
	s_waitcnt lgkmcnt(3)
	v_sub_f32_e32 v76, v103, v32
	s_waitcnt lgkmcnt(1)
	v_sub_f32_e32 v77, v103, v118
	v_min_f32_e32 v76, 0, v76
	v_min_f32_e32 v77, 0, v77
	v_mul_f32_e32 v76, 0x3fb8aa3b, v76
	v_mul_f32_e32 v77, 0x3fb8aa3b, v77
	v_exp_f32_e32 v76, v76
	v_exp_f32_e32 v77, v77
	v_mfma_f32_16x16x32_bf16 v[108:111], v[104:107], v[50:53], v[108:111]
	v_sub_f32_e32 v74, v102, v100
	v_min_f32_e32 v74, 0, v74
	v_mul_f32_e32 v74, 0x3fb8aa3b, v74
	s_waitcnt lgkmcnt(0)
	v_pk_mul_f32 v[76:77], v[90:91], v[76:77]
	v_exp_f32_e32 v119, v74
	v_sub_f32_e32 v74, v102, v101
	s_nop 0
	v_pk_mul_f32 v[76:77], v[76:77], v[110:111]
	v_mfma_f32_16x16x32_bf16 v[110:113], v[82:85], v[46:49], 0
	v_min_f32_e32 v74, 0, v74
	v_mul_f32_e32 v74, 0x3fb8aa3b, v74
	v_exp_f32_e32 v120, v74
	v_mfma_f32_16x16x32_bf16 v[82:85], v[82:85], v[20:23], 0
	v_sub_f32_e32 v74, v102, v32
	v_sub_f32_e32 v75, v102, v118
	v_min_f32_e32 v74, 0, v74
	v_min_f32_e32 v75, 0, v75
	v_mfma_f32_16x16x32_bf16 v[82:85], v[92:95], v[16:19], v[82:85]
	v_mul_f32_e32 v74, 0x3fb8aa3b, v74
	v_mul_f32_e32 v75, 0x3fb8aa3b, v75
	v_exp_f32_e32 v74, v74
	v_exp_f32_e32 v75, v75
	v_mfma_f32_16x16x32_bf16 v[82:85], v[96:99], v[8:11], v[82:85]
	v_mul_f32_e64 v74, v90, v74
	v_mul_f32_e64 v75, v91, v75
	v_mfma_f32_16x16x32_bf16 v[110:113], v[92:95], v[42:45], v[110:113]
	v_mul_f32_e64 v74, v74, v80
	v_mul_f32_e64 v75, v75, v81
	v_sub_f32_e32 v80, v28, v100
	v_min_f32_e32 v80, 0, v80
	v_mfma_f32_16x16x32_bf16 v[92:95], v[104:107], v[12:15], v[82:85]
	v_mul_f32_e32 v80, 0x3fb8aa3b, v80
	v_exp_f32_e32 v116, v80
	v_sub_f32_e32 v80, v28, v101
	v_sub_f32_e32 v82, v29, v100
	v_sub_f32_e32 v83, v29, v101
	v_min_f32_e32 v82, 0, v82
	v_min_f32_e32 v83, 0, v83
	v_mfma_f32_16x16x32_bf16 v[110:113], v[96:99], v[38:41], v[110:113]
	v_mul_f32_e32 v82, 0x3fb8aa3b, v82
	v_mul_f32_e32 v83, 0x3fb8aa3b, v83
	ds_read_b64 v[96:97], v194
	v_min_f32_e32 v80, 0, v80
	v_exp_f32_e32 v82, v82
	v_exp_f32_e32 v83, v83
	v_mul_f32_e32 v80, 0x3fb8aa3b, v80
	v_exp_f32_e32 v117, v80
	v_sub_f32_e32 v80, v28, v32
	v_sub_f32_e32 v32, v29, v32
	v_min_f32_e32 v32, 0, v32
	s_waitcnt lgkmcnt(0)
	v_pk_mul_f32 v[82:83], v[96:97], v[82:83]
	v_mul_f32_e32 v32, 0x3fb8aa3b, v32
	v_sub_f32_e32 v81, v28, v118
	v_pk_mul_f32 v[82:83], v[82:83], v[92:93]
	v_exp_f32_e32 v92, v32
	v_sub_f32_e32 v32, v29, v118
	v_min_f32_e32 v80, 0, v80
	v_min_f32_e32 v81, 0, v81
	v_min_f32_e32 v32, 0, v32
	v_mul_f32_e32 v80, 0x3fb8aa3b, v80
	v_mul_f32_e32 v81, 0x3fb8aa3b, v81
	v_mul_f32_e32 v84, v96, v119
	v_mul_f32_e32 v32, 0x3fb8aa3b, v32
	v_exp_f32_e32 v80, v80
	v_exp_f32_e32 v81, v81
	v_mul_f32_e32 v78, v84, v78
	v_exp_f32_e32 v93, v32
	v_mfma_f32_16x16x32_bf16 v[110:113], v[104:107], v[24:27], v[110:113]
	v_cndmask_b32_e64 v126, v78, 0, s[46:47]
	v_mul_f32_e32 v78, v97, v120
	v_mul_f32_e32 v78, v78, v79
	v_cndmask_b32_e64 v127, 0, v78, s[48:49]
	v_pk_mul_f32 v[78:79], v[96:97], v[114:115]
	v_pk_mul_f32 v[80:81], v[90:91], v[80:81]
	v_pk_mul_f32 v[84:85], v[78:79], v[108:109]
	v_pk_mul_f32 v[78:79], v[96:97], v[116:117]
	v_pk_mul_f32 v[90:91], v[90:91], v[92:93]
	v_pk_mul_f32 v[78:79], v[78:79], v[110:111]
	v_pk_mul_f32 v[90:91], v[90:91], v[94:95]
	global_load_dwordx4 v[92:95], v[30:31], off
	global_load_dwordx4 v[96:99], v[30:31], off offset:64
	global_load_dwordx4 v[104:107], v[30:31], off offset:128
	global_load_dwordx4 v[108:111], v[30:31], off offset:192
	v_pk_mul_f32 v[80:81], v[80:81], v[112:113]
	ds_read_b128 v[112:115], v193 offset:64
	s_waitcnt vmcnt(3)
	v_mfma_f32_16x16x32_bf16 v[116:119], v[92:95], v[62:65], 0
	s_waitcnt lgkmcnt(0)
	v_sub_f32_e32 v30, v103, v112
	v_min_f32_e32 v30, 0, v30
	v_mul_f32_e32 v30, 0x3fb8aa3b, v30
	v_mfma_f32_16x16x32_bf16 v[120:123], v[92:95], v[46:49], 0
	v_exp_f32_e32 v32, v30
	v_sub_f32_e32 v30, v103, v113
	v_min_f32_e32 v30, 0, v30
	v_mfma_f32_16x16x32_bf16 v[92:95], v[92:95], v[20:23], 0
	v_mul_f32_e32 v30, 0x3fb8aa3b, v30
	v_exp_f32_e32 v128, v30
	v_sub_f32_e32 v100, v28, v112
	s_waitcnt vmcnt(2)
	v_mfma_f32_16x16x32_bf16 v[116:119], v[96:99], v[58:61], v[116:119]
	v_sub_f32_e32 v101, v28, v113
	v_min_f32_e32 v100, 0, v100
	v_min_f32_e32 v101, 0, v101
	v_mfma_f32_16x16x32_bf16 v[120:123], v[96:99], v[42:45], v[120:123]
	v_mul_f32_e32 v100, 0x3fb8aa3b, v100
	v_mul_f32_e32 v101, 0x3fb8aa3b, v101
	v_exp_f32_e32 v100, v100
	v_mfma_f32_16x16x32_bf16 v[92:95], v[96:99], v[16:19], v[92:95]
	v_sub_f32_e32 v96, v29, v112
	v_min_f32_e32 v96, 0, v96
	v_mul_f32_e32 v96, 0x3fb8aa3b, v96
	s_waitcnt vmcnt(1)
	v_mfma_f32_16x16x32_bf16 v[116:119], v[104:107], v[54:57], v[116:119]
	v_exp_f32_e32 v101, v101
	v_sub_f32_e32 v30, v103, v114
	v_sub_f32_e32 v31, v103, v115
	v_mfma_f32_16x16x32_bf16 v[120:123], v[104:107], v[38:41], v[120:123]
	v_min_f32_e32 v30, 0, v30
	v_min_f32_e32 v31, 0, v31
	v_sub_f32_e32 v124, v28, v114
	v_mfma_f32_16x16x32_bf16 v[92:95], v[104:107], v[8:11], v[92:95]
	v_exp_f32_e32 v104, v96
	v_sub_f32_e32 v96, v29, v113
	v_min_f32_e32 v96, 0, v96
	v_mul_f32_e32 v96, 0x3fb8aa3b, v96
	v_exp_f32_e32 v105, v96
	ds_read_b128 v[96:99], v194 offset:64
	s_waitcnt vmcnt(0)
	v_mfma_f32_16x16x32_bf16 v[116:119], v[108:111], v[50:53], v[116:119]
	v_sub_f32_e32 v125, v28, v115
	v_mul_f32_e32 v30, 0x3fb8aa3b, v30
	v_mul_f32_e32 v31, 0x3fb8aa3b, v31
	s_waitcnt lgkmcnt(0)
	v_mul_f32_e32 v32, v96, v32
	v_mfma_f32_16x16x32_bf16 v[120:123], v[108:111], v[24:27], v[120:123]
	s_nop 1
	v_mul_f32_e32 v32, v32, v116
	v_pk_mul_f32 v[100:101], v[96:97], v[100:101]
	v_min_f32_e32 v124, 0, v124
	v_mfma_f32_16x16x32_bf16 v[92:95], v[108:111], v[12:15], v[92:95]
	v_cndmask_b32_e64 v108, v32, 0, s[46:47]
	v_mul_f32_e32 v32, v97, v128
	v_mul_f32_e32 v32, v32, v117
	v_cndmask_b32_e64 v109, 0, v32, s[48:49]
	v_sub_f32_e32 v32, v29, v114
	v_min_f32_e32 v32, 0, v32
	v_pk_mul_f32 v[96:97], v[96:97], v[104:105]
	v_mul_f32_e32 v32, 0x3fb8aa3b, v32
	v_min_f32_e32 v125, 0, v125
	v_pk_mul_f32 v[92:93], v[96:97], v[92:93]
	v_exp_f32_e32 v96, v32
	v_sub_f32_e32 v32, v29, v115
	v_exp_f32_e32 v30, v30
	v_exp_f32_e32 v31, v31
	v_mul_f32_e32 v124, 0x3fb8aa3b, v124
	v_mul_f32_e32 v125, 0x3fb8aa3b, v125
	v_min_f32_e32 v32, 0, v32
	v_exp_f32_e32 v124, v124
	v_exp_f32_e32 v125, v125
	v_mul_f32_e32 v32, 0x3fb8aa3b, v32
	v_exp_f32_e32 v97, v32
	v_pk_mul_f32 v[30:31], v[98:99], v[30:31]
	v_pk_mul_f32 v[100:101], v[100:101], v[120:121]
	v_pk_mul_f32 v[104:105], v[30:31], v[118:119]
	v_pk_mul_f32 v[30:31], v[98:99], v[124:125]
	v_cvt_pk_bf16_f32 v78, v78, v79
	v_pk_mul_f32 v[106:107], v[30:31], v[122:123]
	v_pk_mul_f32 v[30:31], v[98:99], v[96:97]
	v_cvt_pk_bf16_f32 v79, v80, v81
	v_pk_mul_f32 v[94:95], v[30:31], v[94:95]
	v_cvt_pk_bf16_f32 v31, v74, v75
	v_cvt_pk_bf16_f32 v75, v76, v77
	v_cvt_pk_bf16_f32 v77, v104, v105
	v_cvt_pk_bf16_f32 v74, v84, v85
	v_cndmask_b32_e64 v84, v77, 0, s[52:53]
	v_lshrrev_b32_e32 v77, 16, v77
	v_cndmask_b32_e64 v77, v77, 0, s[50:51]
	v_perm_b32 v77, v77, v84, s0
	v_cvt_pk_bf16_f32 v80, v100, v101
	v_cvt_pk_bf16_f32 v81, v106, v107
	v_cvt_pk_bf16_f32 v82, v82, v83
	v_cvt_pk_bf16_f32 v83, v90, v91
	v_cvt_pk_bf16_f32 v84, v92, v93
	v_cvt_pk_bf16_f32 v85, v94, v95
	global_load_dwordx4 v[90:93], v[88:89], off
	global_load_dwordx4 v[94:97], v[88:89], off offset:64
	global_load_dwordx4 v[98:101], v[88:89], off offset:128
	global_load_dwordx4 v[104:107], v[88:89], off offset:192
	v_cvt_pk_bf16_f32 v76, v108, v109
	ds_read_b128 v[108:111], v193 offset:128
	s_waitcnt vmcnt(3)
	v_mfma_f32_16x16x32_bf16 v[112:115], v[90:93], v[46:49], 0
	s_waitcnt lgkmcnt(0)
	v_sub_f32_e32 v88, v28, v108
	v_min_f32_e32 v88, 0, v88
	v_mul_f32_e32 v88, 0x3fb8aa3b, v88
	v_exp_f32_e32 v118, v88
	v_sub_f32_e32 v88, v28, v109
	v_min_f32_e32 v88, 0, v88
	v_mul_f32_e32 v88, 0x3fb8aa3b, v88
	v_exp_f32_e32 v119, v88
	v_sub_f32_e32 v88, v28, v110
	v_min_f32_e32 v88, 0, v88
	v_mul_f32_e32 v88, 0x3fb8aa3b, v88
	v_exp_f32_e32 v116, v88
	v_sub_f32_e32 v88, v28, v111
	v_min_f32_e32 v88, 0, v88
	v_mul_f32_e32 v88, 0x3fb8aa3b, v88
	v_exp_f32_e32 v117, v88
	v_mfma_f32_16x16x32_bf16 v[88:91], v[90:93], v[20:23], 0
	v_cndmask_b32_e64 v32, v31, 0, s[52:53]
	v_lshrrev_b32_e32 v31, 16, v31
	v_cndmask_b32_e64 v31, v31, 0, s[50:51]
	s_waitcnt vmcnt(2)
	v_mfma_f32_16x16x32_bf16 v[88:91], v[94:97], v[16:19], v[88:91]
	v_perm_b32 v31, v31, v32, s0
	v_cvt_pk_bf16_f32 v30, v126, v127
	v_mul_f32_e32 v28, 0x3fb8aa3b, v28
	s_waitcnt vmcnt(1)
	v_mfma_f32_16x16x32_bf16 v[88:91], v[98:101], v[8:11], v[88:91]
	v_exp_f32_e32 v178, v28
	v_mul_f32_e32 v28, 0x3fb8aa3b, v29
	v_exp_f32_e32 v28, v28
	s_waitcnt vmcnt(0)
	v_mfma_f32_16x16x32_bf16 v[90:93], v[104:107], v[12:15], v[88:91]
	v_mov_b32_e32 v32, v33
	s_nop 1
	v_sub_f32_e32 v88, v29, v108
	v_sub_f32_e32 v89, v29, v109
	v_mfma_f32_16x16x32_bf16 v[112:115], v[94:97], v[42:45], v[112:115]
	v_min_f32_e32 v88, 0, v88
	v_min_f32_e32 v89, 0, v89
	v_mul_f32_e32 v88, 0x3fb8aa3b, v88
	v_mul_f32_e32 v89, 0x3fb8aa3b, v89
	ds_read_b128 v[94:97], v194 offset:128
	v_exp_f32_e32 v88, v88
	v_exp_f32_e32 v89, v89
	v_mfma_f32_16x16x32_bf16 v[112:115], v[98:101], v[38:41], v[112:115]
	s_waitcnt lgkmcnt(0)
	v_mul_f32_e32 v98, v94, v118
	v_pk_mul_f32 v[88:89], v[94:95], v[88:89]
	v_mfma_f32_16x16x32_bf16 v[112:115], v[104:107], v[24:27], v[112:115]
	v_mul_f32_e64 v90, v88, v90
	v_mul_f32_e64 v91, v89, v91
	v_sub_f32_e32 v88, v29, v110
	v_min_f32_e32 v88, 0, v88
	v_mul_f32_e32 v88, 0x3fb8aa3b, v88
	v_exp_f32_e32 v94, v88
	v_sub_f32_e32 v88, v29, v111
	v_min_f32_e32 v88, 0, v88
	v_mul_f32_e32 v98, v98, v112
	v_mul_f32_e32 v88, 0x3fb8aa3b, v88
	v_cndmask_b32_e64 v120, v98, 0, s[46:47]
	v_mul_f32_e32 v98, v95, v119
	v_exp_f32_e32 v95, v88
	v_mul_f32_e32 v98, v98, v113
	v_cndmask_b32_e64 v121, 0, v98, s[48:49]
	v_pk_mul_f32 v[88:89], v[96:97], v[116:117]
	v_pk_mul_f32 v[94:95], v[96:97], v[94:95]
	v_pk_mul_f32 v[88:89], v[88:89], v[114:115]
	v_pk_mul_f32 v[92:93], v[94:95], v[92:93]
	global_load_dwordx4 v[94:97], v[86:87], off
	global_load_dwordx4 v[98:101], v[86:87], off offset:64
	global_load_dwordx4 v[104:107], v[86:87], off offset:128
	global_load_dwordx4 v[108:111], v[86:87], off offset:192
	s_waitcnt vmcnt(3)
	v_mfma_f32_16x16x32_bf16 v[94:97], v[94:97], v[20:23], 0
	ds_read_b128 v[112:115], v193 offset:192
	ds_read_b128 v[116:119], v194 offset:192
	v_cvt_pk_bf16_f32 v90, v90, v91
	v_cvt_pk_bf16_f32 v91, v92, v93
	s_waitcnt vmcnt(2)
	v_mfma_f32_16x16x32_bf16 v[94:97], v[98:101], v[16:19], v[94:97]
	s_waitcnt lgkmcnt(1)
	v_sub_f32_e32 v86, v29, v112
	v_min_f32_e32 v86, 0, v86
	v_mul_f32_e32 v86, 0x3fb8aa3b, v86
	s_waitcnt vmcnt(1)
	v_mfma_f32_16x16x32_bf16 v[94:97], v[104:107], v[8:11], v[94:97]
	v_exp_f32_e32 v86, v86
	v_sub_f32_e32 v87, v29, v115
	v_min_f32_e32 v87, 0, v87
	s_waitcnt vmcnt(0)
	v_mfma_f32_16x16x32_bf16 v[94:97], v[108:111], v[12:15], v[94:97]
	s_waitcnt lgkmcnt(0)
	v_mul_f32_e32 v86, v116, v86
	v_mul_f32_e32 v87, 0x3fb8aa3b, v87
	v_exp_f32_e32 v87, v87
	s_nop 3
	v_mul_f32_e32 v86, v86, v94
	v_cndmask_b32_e64 v98, v86, 0, s[46:47]
	v_sub_f32_e32 v86, v29, v113
	v_min_f32_e32 v86, 0, v86
	v_mul_f32_e32 v86, 0x3fb8aa3b, v86
	v_exp_f32_e32 v86, v86
	s_nop 0
	v_mul_f32_e32 v86, v117, v86
	v_mul_f32_e32 v86, v86, v95
	v_cndmask_b32_e64 v99, 0, v86, s[48:49]
	v_sub_f32_e32 v86, v29, v114
	v_min_f32_e32 v86, 0, v86
	v_mul_f32_e32 v86, 0x3fb8aa3b, v86
	v_exp_f32_e32 v86, v86
	v_cvt_pk_bf16_f32 v92, v98, v99
	v_mul_f32_e32 v98, 0x3fb8aa3b, v102
	v_mul_f32_e32 v102, 0x3fb8aa3b, v103
	v_pk_mul_f32 v[86:87], v[118:119], v[86:87]
	v_exp_f32_e32 v180, v98
	v_pk_mul_f32 v[94:95], v[86:87], v[96:97]
	v_cvt_pk_bf16_f32 v87, v88, v89
	v_cvt_pk_bf16_f32 v93, v94, v95
	v_cndmask_b32_e64 v88, v87, 0, s[52:53]
	v_lshrrev_b32_e32 v87, 16, v87
	v_cndmask_b32_e64 v94, v93, 0, s[52:53]
	v_lshrrev_b32_e32 v93, 16, v93
	v_cndmask_b32_e64 v87, v87, 0, s[50:51]
	v_cndmask_b32_e64 v93, v93, 0, s[50:51]
	v_perm_b32 v87, v87, v88, s0
	v_perm_b32 v93, v93, v94, s0
	s_lshl_b64 s[0:1], s[20:21], 12
	s_lshl_b64 s[20:21], s[22:23], 6
	s_add_u32 s0, s20, s0
	s_addc_u32 s1, s21, s1
	v_mov_b32_e32 v95, s1
	v_or_b32_e32 v94, s0, v166
	v_lshlrev_b64 v[94:95], 8, v[94:95]
	v_lshl_add_u64 v[142:143], v[164:165], 0, v[94:95]
	v_cvt_pk_bf16_f32 v86, v120, v121
	s_waitcnt vmcnt(3)
	v_mfma_f32_16x16x32_bf16 v[94:97], v[144:147], v[4:7], 0
	v_exp_f32_e32 v176, v102
	s_movk_i32 s0, 0x1000
	v_mfma_f32_16x16x32_bf16 v[98:101], v[144:147], v[62:65], 0
	v_mov_b32_e32 v88, v33
	v_mov_b32_e32 v89, v33
	v_mfma_f32_16x16x32_bf16 v[102:105], v[144:147], v[46:49], 0
	v_mfma_f32_16x16x32_bf16 v[106:109], v[144:147], v[20:23], 0
	s_waitcnt vmcnt(2)
	v_mfma_f32_16x16x32_bf16 v[94:97], v[148:151], v[0:3], v[94:97]
	v_mfma_f32_16x16x32_bf16 v[98:101], v[148:151], v[58:61], v[98:101]
	v_mfma_f32_16x16x32_bf16 v[102:105], v[148:151], v[42:45], v[102:105]
	v_mfma_f32_16x16x32_bf16 v[106:109], v[148:151], v[16:19], v[106:109]
	v_add_co_u32_e64 v110, s[0:1], s0, v142
	s_nop 1
	v_addc_co_u32_e64 v111, s[0:1], 0, v143, s[0:1]
	v_add_co_u32_e64 v126, s[0:1], s56, v142
	s_waitcnt vmcnt(1)
	v_mfma_f32_16x16x32_bf16 v[94:97], v[152:155], v[70:73], v[94:97]
	v_addc_co_u32_e64 v127, s[0:1], 0, v143, s[0:1]
	global_load_dwordx4 v[122:125], v[126:127], off offset:-4096
	global_load_dwordx4 v[128:131], v[110:111], off offset:64
	global_load_dwordx4 v[132:135], v[110:111], off offset:128
	global_load_dwordx4 v[136:139], v[110:111], off offset:192
	v_mfma_f32_16x16x32_bf16 v[98:101], v[152:155], v[54:57], v[98:101]
	v_mfma_f32_16x16x32_bf16 v[102:105], v[152:155], v[38:41], v[102:105]
	v_mfma_f32_16x16x32_bf16 v[106:109], v[152:155], v[8:11], v[106:109]
	s_waitcnt vmcnt(4)
	v_mfma_f32_16x16x32_bf16 v[94:97], v[138:141], v[66:69], v[94:97]
	v_mfma_f32_16x16x32_bf16 v[98:101], v[138:141], v[50:53], v[98:101]
	v_mfma_f32_16x16x32_bf16 v[102:105], v[138:141], v[24:27], v[102:105]
	s_nop 5
	v_mul_f32_e64 v96, v180, v96
	v_mul_f32_e64 v97, v180, v97
	v_pk_mul_f32 v[94:95], v[180:181], v[94:95] op_sel_hi:[0,1]
	v_mfma_f32_16x16x32_bf16 v[106:109], v[138:141], v[12:15], v[106:109]
	s_waitcnt vmcnt(3)
	v_mfma_f32_16x16x32_bf16 v[110:113], v[122:125], v[4:7], 0
	v_mul_f32_e64 v104, v178, v104
	v_mul_f32_e64 v105, v178, v105
	v_pk_mul_f32 v[102:103], v[178:179], v[102:103] op_sel_hi:[0,1]
	s_nop 2
	v_pk_mul_f32 v[108:109], v[28:29], v[108:109] op_sel_hi:[0,1]
	v_mfma_f32_16x16x32_bf16 v[114:117], v[122:125], v[62:65], 0
	v_mul_f32_e64 v106, v28, v106
	v_mul_f32_e64 v107, v28, v107
	v_mfma_f32_16x16x32_bf16 v[118:121], v[122:125], v[46:49], 0
	v_mfma_f32_16x16x32_bf16 v[122:125], v[122:125], v[20:23], 0
	s_waitcnt vmcnt(2)
	v_mfma_f32_16x16x32_bf16 v[110:113], v[128:131], v[0:3], v[110:113]
	v_mfma_f32_16x16x32_bf16 v[114:117], v[128:131], v[58:61], v[114:117]
	v_mfma_f32_16x16x32_bf16 v[118:121], v[128:131], v[42:45], v[118:121]
	v_mfma_f32_16x16x32_bf16 v[122:125], v[128:131], v[16:19], v[122:125]
	s_waitcnt vmcnt(1)
	v_mfma_f32_16x16x32_bf16 v[110:113], v[132:135], v[70:73], v[110:113]
	v_mfma_f32_16x16x32_bf16 v[114:117], v[132:135], v[54:57], v[114:117]
	v_mfma_f32_16x16x32_bf16 v[118:121], v[132:135], v[38:41], v[118:121]
	v_mfma_f32_16x16x32_bf16 v[122:125], v[132:135], v[8:11], v[122:125]
	s_waitcnt vmcnt(0)
	v_mfma_f32_16x16x32_bf16 v[110:113], v[136:139], v[66:69], v[110:113]
	v_mfma_f32_16x16x32_bf16 v[114:117], v[136:139], v[50:53], v[114:117]
	v_mfma_f32_16x16x32_bf16 v[118:121], v[136:139], v[24:27], v[118:121]
	s_nop 5
	v_mul_f32_e64 v112, v180, v112
	v_mul_f32_e64 v113, v180, v113
	v_pk_mul_f32 v[110:111], v[180:181], v[110:111] op_sel_hi:[0,1]
	v_pk_mul_f32 v[116:117], v[176:177], v[116:117] op_sel_hi:[0,1]
	v_mfma_f32_16x16x32_bf16 v[122:125], v[136:139], v[12:15], v[122:125]
	global_load_dwordx4 v[138:141], v[126:127], off
	global_load_dwordx4 v[144:147], v[126:127], off offset:64
	global_load_dwordx4 v[148:151], v[126:127], off offset:128
	global_load_dwordx4 v[152:155], v[126:127], off offset:192
	v_pk_mul_f32 v[114:115], v[176:177], v[114:115] op_sel_hi:[0,1]
	s_waitcnt vmcnt(3)
	v_mfma_f32_16x16x32_bf16 v[126:129], v[138:141], v[4:7], 0
	v_mul_f32_e64 v120, v178, v120
	v_mul_f32_e64 v121, v178, v121
	v_pk_mul_f32 v[118:119], v[178:179], v[118:119] op_sel_hi:[0,1]
	v_pk_mul_f32 v[124:125], v[28:29], v[124:125] op_sel_hi:[0,1]
	v_mfma_f32_16x16x32_bf16 v[130:133], v[138:141], v[62:65], 0
	v_mul_f32_e64 v122, v28, v122
	v_mul_f32_e64 v123, v28, v123
	v_mfma_f32_16x16x32_bf16 v[134:137], v[138:141], v[46:49], 0
	v_mfma_f32_16x16x32_bf16 v[138:141], v[138:141], v[20:23], 0
	s_waitcnt vmcnt(2)
	v_mfma_f32_16x16x32_bf16 v[126:129], v[144:147], v[0:3], v[126:129]
	v_mfma_f32_16x16x32_bf16 v[130:133], v[144:147], v[58:61], v[130:133]
	v_mfma_f32_16x16x32_bf16 v[134:137], v[144:147], v[42:45], v[134:137]
	v_mfma_f32_16x16x32_bf16 v[138:141], v[144:147], v[16:19], v[138:141]
	s_waitcnt vmcnt(1)
	v_mfma_f32_16x16x32_bf16 v[126:129], v[148:151], v[70:73], v[126:129]
	v_mfma_f32_16x16x32_bf16 v[130:133], v[148:151], v[54:57], v[130:133]
	v_mfma_f32_16x16x32_bf16 v[134:137], v[148:151], v[38:41], v[134:137]
	v_mfma_f32_16x16x32_bf16 v[138:141], v[148:151], v[8:11], v[138:141]
	s_waitcnt vmcnt(0)
	v_mfma_f32_16x16x32_bf16 v[126:129], v[152:155], v[66:69], v[126:129]
	v_mfma_f32_16x16x32_bf16 v[130:133], v[152:155], v[50:53], v[130:133]
	v_mfma_f32_16x16x32_bf16 v[134:137], v[152:155], v[24:27], v[134:137]
	s_nop 5
	v_mul_f32_e64 v128, v180, v128
	v_mul_f32_e64 v129, v180, v129
	v_pk_mul_f32 v[126:127], v[180:181], v[126:127] op_sel_hi:[0,1]
	v_pk_mul_f32 v[132:133], v[176:177], v[132:133] op_sel_hi:[0,1]
	v_mfma_f32_16x16x32_bf16 v[138:141], v[152:155], v[12:15], v[138:141]
	v_add_co_u32_e64 v154, s[0:1], s77, v142
	v_pk_mul_f32 v[130:131], v[176:177], v[130:131] op_sel_hi:[0,1]
	s_nop 0
	v_addc_co_u32_e64 v155, s[0:1], 0, v143, s[0:1]
	global_load_dwordx4 v[142:145], v[154:155], off
	global_load_dwordx4 v[146:149], v[154:155], off offset:64
	global_load_dwordx4 v[150:153], v[154:155], off offset:128
	s_nop 0
	global_load_dwordx4 v[154:157], v[154:155], off offset:192
	s_waitcnt vmcnt(3)
	v_mfma_f32_16x16x32_bf16 v[4:7], v[142:145], v[4:7], 0
	v_mul_f32_e64 v136, v178, v136
	v_mul_f32_e64 v137, v178, v137
	v_pk_mul_f32 v[134:135], v[178:179], v[134:135] op_sel_hi:[0,1]
	s_waitcnt vmcnt(2)
	v_mfma_f32_16x16x32_bf16 v[0:3], v[146:149], v[0:3], v[4:7]
	v_mul_f32_e64 v140, v28, v140
	v_mul_f32_e64 v141, v28, v141
	v_pk_mul_f32 v[138:139], v[28:29], v[138:139] op_sel_hi:[0,1]
	s_add_u32 s0, s30, s18
	s_waitcnt vmcnt(1)
	v_mfma_f32_16x16x32_bf16 v[0:3], v[150:153], v[70:73], v[0:3]
	s_addc_u32 s1, s31, s19
	s_waitcnt vmcnt(0)
	v_mfma_f32_16x16x32_bf16 v[0:3], v[154:157], v[66:69], v[0:3]
	s_nop 7
	v_pk_mul_f32 v[68:69], v[180:181], v[2:3] op_sel_hi:[0,1]
	v_pk_mul_f32 v[66:67], v[180:181], v[0:1] op_sel_hi:[0,1]
	v_mfma_f32_16x16x32_bf16 v[0:3], v[142:145], v[62:65], 0
	v_mfma_f32_16x16x32_bf16 v[0:3], v[146:149], v[58:61], v[0:3]
	v_mfma_f32_16x16x32_bf16 v[0:3], v[150:153], v[54:57], v[0:3]
	v_mfma_f32_16x16x32_bf16 v[0:3], v[154:157], v[50:53], v[0:3]
	s_nop 7
	v_pk_mul_f32 v[72:73], v[176:177], v[2:3] op_sel_hi:[0,1]
	v_pk_mul_f32 v[70:71], v[176:177], v[0:1] op_sel_hi:[0,1]
	v_mfma_f32_16x16x32_bf16 v[0:3], v[142:145], v[46:49], 0
	v_mfma_f32_16x16x32_bf16 v[0:3], v[146:149], v[42:45], v[0:3]
	v_mfma_f32_16x16x32_bf16 v[0:3], v[150:153], v[38:41], v[0:3]
	v_mfma_f32_16x16x32_bf16 v[0:3], v[154:157], v[24:27], v[0:3]
	s_nop 7
	v_pk_mul_f32 v[26:27], v[178:179], v[2:3] op_sel_hi:[0,1]
	v_pk_mul_f32 v[24:25], v[178:179], v[0:1] op_sel_hi:[0,1]
	v_mfma_f32_16x16x32_bf16 v[0:3], v[142:145], v[20:23], 0
	v_mfma_f32_16x16x32_bf16 v[0:3], v[146:149], v[16:19], v[0:3]
	v_mul_f32_e64 v18, v176, v100
	v_mul_f32_e64 v19, v176, v101
	v_pk_mul_f32 v[16:17], v[176:177], v[98:99] op_sel_hi:[0,1]
	v_mfma_f32_16x16x32_bf16 v[0:3], v[150:153], v[8:11], v[0:3]
	v_mfma_f32_16x16x32_bf16 v[0:3], v[154:157], v[12:15], v[0:3]
	s_nop 7
	v_pk_mul_f32 v[10:11], v[28:29], v[2:3] op_sel_hi:[0,1]
	v_pk_mul_f32 v[8:9], v[28:29], v[0:1] op_sel_hi:[0,1]
	ds_read_b64_tr_b16 v[2:3], v214 offset:2560
	ds_read_b64_tr_b16 v[0:1], v214
	ds_read_b64_tr_b16 v[4:5], v214 offset:32
	ds_read_b64_tr_b16 v[12:13], v214 offset:5120
	ds_read_b64_tr_b16 v[14:15], v214 offset:7680
	s_waitcnt lgkmcnt(3)
	v_mfma_f32_16x16x32_bf16 v[94:97], v[0:3], v[30:33], v[94:97]
	v_mfma_f32_16x16x32_bf16 v[50:53], v[0:3], v[74:77], v[16:19]
	v_mfma_f32_16x16x32_bf16 v[16:19], v[0:3], v[78:81], v[102:105]
	v_mfma_f32_16x16x32_bf16 v[0:3], v[0:3], v[82:85], v[106:109]
	s_waitcnt lgkmcnt(0)
	v_mfma_f32_16x16x32_bf16 v[38:41], v[12:15], v[86:89], v[16:19]
	v_mfma_f32_16x16x32_bf16 v[12:15], v[12:15], v[90:93], v[0:3]
	ds_read_b64_tr_b16 v[6:7], v214 offset:2592
	s_nop 3
	ds_read_b64_tr_b16 v[0:1], v214 offset:5152
	ds_read_b64_tr_b16 v[2:3], v214 offset:7712
	s_waitcnt lgkmcnt(2)
	v_mfma_f32_16x16x32_bf16 v[62:65], v[4:7], v[30:33], v[110:113]
	v_mfma_f32_16x16x32_bf16 v[46:49], v[4:7], v[74:77], v[114:117]
	v_mfma_f32_16x16x32_bf16 v[16:19], v[4:7], v[78:81], v[118:121]
	v_mfma_f32_16x16x32_bf16 v[4:7], v[4:7], v[82:85], v[122:125]
	s_waitcnt lgkmcnt(0)
	v_mfma_f32_16x16x32_bf16 v[20:23], v[0:3], v[86:89], v[16:19]
	v_mfma_f32_16x16x32_bf16 v[4:7], v[0:3], v[90:93], v[4:7]
	ds_read_b64_tr_b16 v[0:1], v214 offset:64
	ds_read_b64_tr_b16 v[2:3], v214 offset:2624
	ds_read_b64_tr_b16 v[54:55], v214 offset:5184
	ds_read_b64_tr_b16 v[56:57], v214 offset:7744
	ds_read_b64_tr_b16 v[98:99], v214 offset:96
	ds_read_b64_tr_b16 v[100:101], v214 offset:2656
	ds_read_b64_tr_b16 v[102:103], v214 offset:5216
	ds_read_b64_tr_b16 v[104:105], v214 offset:7776
	s_waitcnt lgkmcnt(6)
	v_mfma_f32_16x16x32_bf16 v[58:61], v[0:3], v[30:33], v[126:129]
	v_mfma_f32_16x16x32_bf16 v[42:45], v[0:3], v[74:77], v[130:133]
	v_mfma_f32_16x16x32_bf16 v[16:19], v[0:3], v[78:81], v[134:137]
	v_mfma_f32_16x16x32_bf16 v[0:3], v[0:3], v[82:85], v[138:141]
	s_waitcnt lgkmcnt(4)
	v_mfma_f32_16x16x32_bf16 v[16:19], v[54:57], v[86:89], v[16:19]
	v_mfma_f32_16x16x32_bf16 v[0:3], v[54:57], v[90:93], v[0:3]
	s_waitcnt lgkmcnt(2)
	v_mfma_f32_16x16x32_bf16 v[54:57], v[98:101], v[30:33], v[66:69]
	v_add_u32_e32 v32, v209, v160
	v_mfma_f32_16x16x32_bf16 v[28:31], v[98:101], v[74:77], v[70:73]
	s_nop 0
	ds_read_b64 v[68:69], v32
	s_nop 0
	global_load_dword v70, v33, s[0:1]
	s_add_u32 s0, s2, s16
	s_addc_u32 s1, s3, s17
	v_mfma_f32_16x16x32_bf16 v[24:27], v[98:101], v[78:81], v[24:27]
	v_mov_b64_e32 v[78:79], s[0:1]
	v_mad_i64_i32 v[66:67], s[0:1], v174, s96, v[78:79]
	v_lshl_add_u64 v[72:73], v[66:67], 0, v[172:173]
	global_load_dwordx2 v[74:75], v[72:73], off
	global_load_dwordx2 v[202:203], v[72:73], off offset:32
	global_load_dwordx2 v[216:217], v[72:73], off offset:64
	global_load_dwordx2 v[248:249], v[72:73], off offset:96
	s_waitcnt lgkmcnt(0)
	v_lshlrev_b32_e32 v66, 16, v68
	v_and_b32_e32 v67, 0xffff0000, v68
	v_lshlrev_b32_e32 v68, 16, v69
	v_and_b32_e32 v69, 0xffff0000, v69
	v_mfma_f32_16x16x32_bf16 v[8:11], v[98:101], v[82:85], v[8:11]
	s_waitcnt vmcnt(4)
	v_pk_fma_f32 v[66:67], v[70:71], v[66:67], v[94:95] op_sel_hi:[0,1,1]
	v_pk_fma_f32 v[68:69], v[70:71], v[68:69], v[96:97] op_sel_hi:[0,1,1]
	v_mfma_f32_16x16x32_bf16 v[24:27], v[102:105], v[86:89], v[24:27]
	s_waitcnt vmcnt(3)
	v_lshlrev_b32_e32 v76, 16, v74
	v_mul_f32_e32 v32, 0xbfb8aa3b, v76
	v_exp_f32_e32 v32, v32
	v_and_b32_e32 v77, 0xffff0000, v74
	v_pk_mul_f32 v[66:67], v[66:67], v[76:77]
	v_lshlrev_b32_e32 v74, 16, v75
	v_add_f32_e32 v32, 1.0, v32
	v_rcp_f32_e32 v80, v32
	v_mul_f32_e32 v32, 0xbfb8aa3b, v77
	v_exp_f32_e32 v32, v32
	v_and_b32_e32 v75, 0xffff0000, v75
	v_pk_mul_f32 v[68:69], v[68:69], v[74:75]
	v_mfma_f32_16x16x32_bf16 v[8:11], v[102:105], v[90:93], v[8:11]
	v_add_f32_e32 v32, 1.0, v32
	v_rcp_f32_e32 v81, v32
	s_nop 0
	v_pk_mul_f32 v[66:67], v[66:67], v[80:81]
	s_nop 0
	v_mul_f32_e32 v32, v67, v67
	v_pk_fma_f32 v[76:77], v[66:67], v[66:67], v[32:33] op_sel_hi:[1,1,0]
	v_mul_f32_e32 v32, 0xbfb8aa3b, v74
	v_exp_f32_e32 v32, v32
	s_nop 0
	v_add_f32_e32 v32, 1.0, v32
	v_rcp_f32_e32 v80, v32
	v_mul_f32_e32 v32, 0xbfb8aa3b, v75
	v_exp_f32_e32 v32, v32
	s_nop 0
	v_add_f32_e32 v32, 1.0, v32
	v_rcp_f32_e32 v81, v32
	s_nop 0
	v_pk_mul_f32 v[68:69], v[68:69], v[80:81]
	v_pk_fma_f32 v[74:75], v[68:69], v[68:69], v[76:77]
	v_mul_f32_e32 v32, v69, v69
	v_pk_add_f32 v[74:75], v[32:33], v[74:75] op_sel_hi:[0,1]
	v_add_u32_e32 v32, v209, v189
	ds_read_b64 v[76:77], v32
	s_waitcnt lgkmcnt(0)
	v_lshlrev_b32_e32 v82, 16, v76
	v_and_b32_e32 v83, 0xffff0000, v76
	v_pk_fma_f32 v[62:63], v[70:71], v[82:83], v[62:63] op_sel_hi:[0,1,1]
	v_lshlrev_b32_e32 v76, 16, v77
	v_and_b32_e32 v77, 0xffff0000, v77
	v_pk_fma_f32 v[64:65], v[70:71], v[76:77], v[64:65] op_sel_hi:[0,1,1]
	s_waitcnt vmcnt(2)
	v_mov_b64_e32 v[80:81], v[202:203]
	v_lshlrev_b32_e32 v84, 16, v80
	v_mul_f32_e32 v32, 0xbfb8aa3b, v84
	v_exp_f32_e32 v32, v32
	v_and_b32_e32 v85, 0xffff0000, v80
	v_pk_mul_f32 v[62:63], v[62:63], v[84:85]
	v_lshlrev_b32_e32 v80, 16, v81
	v_add_f32_e32 v32, 1.0, v32
	v_rcp_f32_e32 v86, v32
	v_mul_f32_e32 v32, 0xbfb8aa3b, v85
	v_exp_f32_e32 v32, v32
	v_and_b32_e32 v81, 0xffff0000, v81
	v_pk_mul_f32 v[64:65], v[64:65], v[80:81]
	v_add_f32_e32 v32, 1.0, v32
	v_rcp_f32_e32 v87, v32
	s_nop 0
	v_pk_mul_f32 v[62:63], v[62:63], v[86:87]
	s_nop 0
	v_pk_fma_f32 v[74:75], v[62:63], v[62:63], v[74:75]
	v_mul_f32_e32 v32, v63, v63
	v_pk_add_f32 v[74:75], v[32:33], v[74:75] op_sel_hi:[0,1]
	v_mul_f32_e32 v32, 0xbfb8aa3b, v80
	v_exp_f32_e32 v32, v32
	s_nop 0
	v_add_f32_e32 v32, 1.0, v32
	v_rcp_f32_e32 v82, v32
	v_mul_f32_e32 v32, 0xbfb8aa3b, v81
	v_exp_f32_e32 v32, v32
	s_waitcnt vmcnt(1)
	v_mov_b64_e32 v[80:81], v[216:217]
	v_lshlrev_b32_e32 v84, 16, v80
	v_add_f32_e32 v32, 1.0, v32
	v_rcp_f32_e32 v83, v32
	v_and_b32_e32 v85, 0xffff0000, v80
	v_lshlrev_b32_e32 v80, 16, v81
	v_and_b32_e32 v81, 0xffff0000, v81
	v_pk_mul_f32 v[64:65], v[64:65], v[82:83]
	s_nop 0
	v_pk_fma_f32 v[74:75], v[64:65], v[64:65], v[74:75]
	v_mul_f32_e32 v32, v65, v65
	v_pk_add_f32 v[74:75], v[32:33], v[74:75] op_sel_hi:[0,1]
	v_add_u32_e32 v32, v209, v188
	ds_read_b64 v[76:77], v32
	v_mul_f32_e32 v32, 0xbfb8aa3b, v84
	v_exp_f32_e32 v32, v32
	s_waitcnt lgkmcnt(0)
	v_lshlrev_b32_e32 v82, 16, v76
	v_add_f32_e32 v32, 1.0, v32
	v_rcp_f32_e32 v86, v32
	v_mul_f32_e32 v32, 0xbfb8aa3b, v85
	v_exp_f32_e32 v32, v32
	v_and_b32_e32 v83, 0xffff0000, v76
	v_pk_fma_f32 v[58:59], v[70:71], v[82:83], v[58:59] op_sel_hi:[0,1,1]
	v_pk_mul_f32 v[58:59], v[58:59], v[84:85]
	v_add_f32_e32 v32, 1.0, v32
	v_rcp_f32_e32 v87, v32
	v_lshlrev_b32_e32 v76, 16, v77
	v_and_b32_e32 v77, 0xffff0000, v77
	v_pk_fma_f32 v[60:61], v[70:71], v[76:77], v[60:61] op_sel_hi:[0,1,1]
	v_pk_mul_f32 v[58:59], v[58:59], v[86:87]
	v_pk_mul_f32 v[60:61], v[60:61], v[80:81]
	v_pk_fma_f32 v[74:75], v[58:59], v[58:59], v[74:75]
	v_mul_f32_e32 v32, v59, v59
	v_pk_add_f32 v[74:75], v[32:33], v[74:75] op_sel_hi:[0,1]
	v_mul_f32_e32 v32, 0xbfb8aa3b, v80
	v_exp_f32_e32 v32, v32
	s_nop 0
	v_add_f32_e32 v32, 1.0, v32
	v_rcp_f32_e32 v82, v32
	v_mul_f32_e32 v32, 0xbfb8aa3b, v81
	v_exp_f32_e32 v32, v32
	s_nop 0
	v_add_f32_e32 v32, 1.0, v32
	v_rcp_f32_e32 v83, v32
	s_nop 0
	v_pk_mul_f32 v[60:61], v[60:61], v[82:83]
	s_nop 0
	v_pk_fma_f32 v[74:75], v[60:61], v[60:61], v[74:75]
	v_mul_f32_e32 v32, v61, v61
	v_pk_add_f32 v[74:75], v[32:33], v[74:75] op_sel_hi:[0,1]
	v_add_u32_e32 v32, v209, v187
	ds_read_b64 v[76:77], v32
	s_waitcnt lgkmcnt(0)
	v_lshlrev_b32_e32 v72, 16, v76
	v_and_b32_e32 v73, 0xffff0000, v76
	v_pk_fma_f32 v[54:55], v[70:71], v[72:73], v[54:55] op_sel_hi:[0,1,1]
	s_waitcnt vmcnt(0)
	v_mov_b64_e32 v[80:81], v[248:249]
	v_lshlrev_b32_e32 v82, 16, v80
	v_mul_f32_e32 v32, 0xbfb8aa3b, v82
	v_exp_f32_e32 v32, v32
	v_and_b32_e32 v83, 0xffff0000, v80
	v_pk_mul_f32 v[54:55], v[54:55], v[82:83]
	v_lshlrev_b32_e32 v76, 16, v81
	v_add_f32_e32 v32, 1.0, v32
	v_rcp_f32_e32 v84, v32
	v_mul_f32_e32 v32, 0xbfb8aa3b, v83
	v_exp_f32_e32 v32, v32
	s_nop 0
	v_add_f32_e32 v32, 1.0, v32
	v_rcp_f32_e32 v85, v32
	s_nop 0
	v_pk_mul_f32 v[72:73], v[54:55], v[84:85]
	s_nop 0
	v_pk_fma_f32 v[54:55], v[72:73], v[72:73], v[74:75]
	v_mul_f32_e32 v32, v73, v73
	v_pk_add_f32 v[54:55], v[32:33], v[54:55] op_sel_hi:[0,1]
	v_mul_f32_e32 v32, 0xbfb8aa3b, v76
	v_exp_f32_e32 v32, v32
	v_lshlrev_b32_e32 v74, 16, v77
	v_and_b32_e32 v75, 0xffff0000, v77
	v_and_b32_e32 v77, 0xffff0000, v81
	v_add_f32_e32 v32, 1.0, v32
	v_rcp_f32_e32 v80, v32
	v_mul_f32_e32 v32, 0xbfb8aa3b, v77
	v_exp_f32_e32 v32, v32
	v_pk_fma_f32 v[56:57], v[70:71], v[74:75], v[56:57] op_sel_hi:[0,1,1]
	v_pk_mul_f32 v[56:57], v[56:57], v[76:77]
	v_or_b32_e32 v76, s55, v185
	v_add_f32_e32 v32, 1.0, v32
	v_rcp_f32_e32 v81, v32
	s_nop 0
	v_pk_mul_f32 v[56:57], v[56:57], v[80:81]
	s_nop 0
	v_pk_fma_f32 v[54:55], v[56:57], v[56:57], v[54:55]
	v_mul_f32_e32 v32, v57, v57
	v_pk_add_f32 v[110:111], v[32:33], v[54:55] op_sel_hi:[0,1]
	v_or_b32_e32 v54, s55, v184
	v_mad_i64_i32 v[74:75], s[0:1], v54, s96, v[78:79]
	v_lshl_add_u64 v[74:75], v[74:75], 0, v[172:173]
	global_load_dwordx2 v[126:127], v[74:75], off
	global_load_dwordx2 v[122:123], v[74:75], off offset:32
	global_load_dwordx2 v[116:117], v[74:75], off offset:64
	global_load_dwordx2 v[112:113], v[74:75], off offset:96
	v_mad_i64_i32 v[74:75], s[0:1], v76, s96, v[78:79]
	v_lshl_add_u64 v[74:75], v[74:75], 0, v[172:173]
	global_load_dwordx2 v[106:107], v[74:75], off
	global_load_dwordx2 v[102:103], v[74:75], off offset:32
	global_load_dwordx2 v[98:99], v[74:75], off offset:64
	global_load_dwordx2 v[94:95], v[74:75], off offset:96
	v_or_b32_e32 v74, s55, v186
	v_mad_i64_i32 v[78:79], s[0:1], v74, s96, v[78:79]
	v_lshl_add_u64 v[78:79], v[78:79], 0, v[172:173]
	global_load_dwordx2 v[90:91], v[78:79], off
	global_load_dwordx2 v[86:87], v[78:79], off offset:32
	global_load_dwordx2 v[82:83], v[78:79], off offset:64
	v_add_u32_e32 v32, v211, v160
	global_load_dwordx2 v[78:79], v[78:79], off offset:96
	ds_read_b64 v[120:121], v32
	v_add_u32_e32 v32, v211, v189
	ds_read_b64 v[124:125], v32
	v_add_u32_e32 v32, v211, v188
	ds_read_b64 v[118:119], v32
	v_add_u32_e32 v32, v211, v187
	ds_read_b64 v[114:115], v32
	v_add_u32_e32 v32, v212, v160
	ds_read_b64 v[108:109], v32
	v_add_u32_e32 v32, v212, v189
	ds_read_b64 v[104:105], v32
	v_add_u32_e32 v32, v212, v188
	ds_read_b64 v[100:101], v32
	v_add_u32_e32 v32, v212, v187
	ds_read_b64 v[96:97], v32
	v_add_u32_e32 v32, v210, v160
	ds_read_b64 v[92:93], v32
	v_add_u32_e32 v32, v210, v189
	ds_read_b64 v[88:89], v32
	v_add_u32_e32 v32, v210, v188
	ds_read_b64 v[84:85], v32
	v_add_u32_e32 v32, v210, v187
	ds_read_b64 v[80:81], v32
	s_lshl_b32 s0, s33, 11
	v_mov_b32_e32 v55, v110
	s_add_i32 s16, s0, 0
	s_nop 0
	v_permlane16_swap_b32_e32 v110, v55
	s_add_i32 s16, s16, 0x15000
	v_add_f32_e32 v55, v110, v55
	s_add_i32 s0, s16, s35
	v_mov_b32_e32 v71, v55
	v_lshl_add_u32 v32, v166, 2, s0
	s_nop 0
	v_permlane32_swap_b32_e32 v55, v71
	s_and_saveexec_b64 s[0:1], s[42:43]
	v_add_f32_e32 v55, v55, v71
	ds_write_b32 v32, v55
	s_or_b64 exec, exec, s[0:1]
	s_waitcnt vmcnt(11)
	v_lshlrev_b32_e32 v128, 16, v126
	v_mul_f32_e32 v55, 0xbfb8aa3b, v128
	v_exp_f32_e32 v55, v55
	v_and_b32_e32 v129, 0xffff0000, v126
	v_lshlrev_b32_e32 v126, 16, v127
	v_mov_b32_e32 v71, v70
	v_add_f32_e32 v55, 1.0, v55
	v_rcp_f32_e32 v130, v55
	v_mul_f32_e32 v55, 0xbfb8aa3b, v129
	v_exp_f32_e32 v55, v55
	s_waitcnt lgkmcnt(11)
	v_lshlrev_b32_e32 v110, 16, v120
	v_and_b32_e32 v111, 0xffff0000, v120
	v_pk_fma_f32 v[50:51], v[70:71], v[110:111], v[50:51]
	v_add_f32_e32 v55, 1.0, v55
	v_rcp_f32_e32 v131, v55
	v_mul_f32_e32 v55, 0xbfb8aa3b, v126
	v_exp_f32_e32 v55, v55
	v_and_b32_e32 v127, 0xffff0000, v127
	v_pk_mul_f32 v[50:51], v[50:51], v[128:129]
	v_lshlrev_b32_e32 v120, 16, v121
	v_add_f32_e32 v55, 1.0, v55
	v_rcp_f32_e32 v128, v55
	v_mul_f32_e32 v55, 0xbfb8aa3b, v127
	v_exp_f32_e32 v55, v55
	v_and_b32_e32 v121, 0xffff0000, v121
	v_pk_fma_f32 v[52:53], v[70:71], v[120:121], v[52:53]
	v_pk_mul_f32 v[50:51], v[50:51], v[130:131]
	v_pk_mul_f32 v[52:53], v[52:53], v[126:127]
	v_add_f32_e32 v55, 1.0, v55
	s_waitcnt vmcnt(10)
	v_lshlrev_b32_e32 v126, 16, v122
	v_rcp_f32_e32 v129, v55
	v_mul_f32_e32 v55, 0xbfb8aa3b, v126
	v_exp_f32_e32 v55, v55
	v_and_b32_e32 v127, 0xffff0000, v122
	v_pk_mul_f32 v[52:53], v[52:53], v[128:129]
	v_lshlrev_b32_e32 v122, 16, v123
	v_add_f32_e32 v55, 1.0, v55
	v_rcp_f32_e32 v128, v55
	v_mul_f32_e32 v55, 0xbfb8aa3b, v127
	v_exp_f32_e32 v55, v55
	v_mul_f32_e32 v110, v51, v51
	v_pk_fma_f32 v[110:111], v[50:51], v[50:51], v[110:111] op_sel_hi:[1,1,0]
	v_mul_f32_e32 v120, v53, v53
	v_add_f32_e32 v55, 1.0, v55
	v_rcp_f32_e32 v129, v55
	v_mul_f32_e32 v55, 0xbfb8aa3b, v122
	v_exp_f32_e32 v55, v55
	v_pk_fma_f32 v[110:111], v[52:53], v[52:53], v[110:111]
	v_and_b32_e32 v123, 0xffff0000, v123
	v_pk_add_f32 v[110:111], v[120:121], v[110:111] op_sel_hi:[0,1]
	s_waitcnt lgkmcnt(10)
	v_lshlrev_b32_e32 v120, 16, v124
	v_and_b32_e32 v121, 0xffff0000, v124
	v_pk_fma_f32 v[46:47], v[70:71], v[120:121], v[46:47]
	v_add_f32_e32 v55, 1.0, v55
	v_pk_mul_f32 v[46:47], v[46:47], v[126:127]
	v_rcp_f32_e32 v124, v55
	v_mul_f32_e32 v55, 0xbfb8aa3b, v123
	v_pk_mul_f32 v[46:47], v[46:47], v[128:129]
	v_exp_f32_e32 v55, v55
	v_pk_fma_f32 v[110:111], v[46:47], v[46:47], v[110:111]
	v_mul_f32_e32 v120, v47, v47
	v_pk_add_f32 v[110:111], v[120:121], v[110:111] op_sel_hi:[0,1]
	v_lshlrev_b32_e32 v120, 16, v125
	v_and_b32_e32 v121, 0xffff0000, v125
	v_pk_fma_f32 v[48:49], v[70:71], v[120:121], v[48:49]
	v_add_f32_e32 v55, 1.0, v55
	v_pk_mul_f32 v[48:49], v[48:49], v[122:123]
	s_waitcnt vmcnt(9)
	v_lshlrev_b32_e32 v122, 16, v116
	v_rcp_f32_e32 v125, v55
	v_mul_f32_e32 v55, 0xbfb8aa3b, v122
	v_exp_f32_e32 v55, v55
	v_and_b32_e32 v123, 0xffff0000, v116
	v_pk_mul_f32 v[48:49], v[48:49], v[124:125]
	v_add_f32_e32 v55, 1.0, v55
	v_rcp_f32_e32 v124, v55
	v_mul_f32_e32 v55, 0xbfb8aa3b, v123
	v_exp_f32_e32 v55, v55
	v_pk_fma_f32 v[110:111], v[48:49], v[48:49], v[110:111]
	v_mul_f32_e32 v120, v49, v49
	v_pk_add_f32 v[110:111], v[120:121], v[110:111] op_sel_hi:[0,1]
	v_add_f32_e32 v55, 1.0, v55
	v_rcp_f32_e32 v125, v55
	s_waitcnt lgkmcnt(9)
	v_lshlrev_b32_e32 v120, 16, v118
	v_and_b32_e32 v121, 0xffff0000, v118
	v_pk_fma_f32 v[42:43], v[70:71], v[120:121], v[42:43]
	v_lshlrev_b32_e32 v118, 16, v119
	v_pk_mul_f32 v[42:43], v[42:43], v[122:123]
	v_and_b32_e32 v119, 0xffff0000, v119
	v_pk_mul_f32 v[42:43], v[42:43], v[124:125]
	v_pk_fma_f32 v[44:45], v[70:71], v[118:119], v[44:45]
	v_pk_fma_f32 v[110:111], v[42:43], v[42:43], v[110:111]
	v_mul_f32_e32 v116, v43, v43
	v_pk_add_f32 v[110:111], v[116:117], v[110:111] op_sel_hi:[0,1]
	v_lshlrev_b32_e32 v116, 16, v117
	v_mul_f32_e32 v55, 0xbfb8aa3b, v116
	v_exp_f32_e32 v55, v55
	v_and_b32_e32 v117, 0xffff0000, v117
	s_waitcnt vmcnt(8)
	v_lshlrev_b32_e32 v118, 16, v112
	v_pk_mul_f32 v[44:45], v[44:45], v[116:117]
	v_add_f32_e32 v55, 1.0, v55
	v_rcp_f32_e32 v120, v55
	v_mul_f32_e32 v55, 0xbfb8aa3b, v117
	v_exp_f32_e32 v55, v55
	v_and_b32_e32 v119, 0xffff0000, v112
	v_add_f32_e32 v55, 1.0, v55
	v_rcp_f32_e32 v121, v55
	v_mul_f32_e32 v55, 0xbfb8aa3b, v118
	v_exp_f32_e32 v55, v55
	v_pk_mul_f32 v[44:45], v[44:45], v[120:121]
	s_nop 0
	v_pk_fma_f32 v[110:111], v[44:45], v[44:45], v[110:111]
	v_add_f32_e32 v55, 1.0, v55
	v_rcp_f32_e32 v120, v55
	v_mul_f32_e32 v55, 0xbfb8aa3b, v119
	v_exp_f32_e32 v55, v55
	v_mul_f32_e32 v116, v45, v45
	v_pk_add_f32 v[110:111], v[116:117], v[110:111] op_sel_hi:[0,1]
	s_waitcnt lgkmcnt(8)
	v_lshlrev_b32_e32 v116, 16, v114
	v_add_f32_e32 v55, 1.0, v55
	v_rcp_f32_e32 v121, v55
	v_and_b32_e32 v117, 0xffff0000, v114
	v_pk_fma_f32 v[28:29], v[70:71], v[116:117], v[28:29]
	v_lshlrev_b32_e32 v114, 16, v115
	v_pk_mul_f32 v[28:29], v[28:29], v[118:119]
	v_and_b32_e32 v115, 0xffff0000, v115
	v_pk_mul_f32 v[28:29], v[28:29], v[120:121]
	v_pk_fma_f32 v[30:31], v[70:71], v[114:115], v[30:31]
	v_pk_fma_f32 v[110:111], v[28:29], v[28:29], v[110:111]
	v_mul_f32_e32 v112, v29, v29
	v_pk_add_f32 v[110:111], v[112:113], v[110:111] op_sel_hi:[0,1]
	v_lshlrev_b32_e32 v112, 16, v113
	v_mul_f32_e32 v55, 0xbfb8aa3b, v112
	v_exp_f32_e32 v55, v55
	v_and_b32_e32 v113, 0xffff0000, v113
	v_pk_mul_f32 v[30:31], v[30:31], v[112:113]
	v_add_f32_e32 v55, 1.0, v55
	v_rcp_f32_e32 v116, v55
	v_mul_f32_e32 v55, 0xbfb8aa3b, v113
	v_exp_f32_e32 v55, v55
	s_nop 0
	v_add_f32_e32 v55, 1.0, v55
	v_rcp_f32_e32 v117, v55
	s_nop 0
	v_pk_mul_f32 v[30:31], v[30:31], v[116:117]
	s_nop 0
	v_pk_fma_f32 v[110:111], v[30:31], v[30:31], v[110:111]
	v_mul_f32_e32 v112, v31, v31
	v_pk_add_f32 v[110:111], v[112:113], v[110:111] op_sel_hi:[0,1]
	v_mov_b32_e32 v55, v110
	s_nop 1
	v_permlane16_swap_b32_e32 v110, v55
	v_add_f32_e32 v55, v110, v55
	v_mov_b32_e32 v75, v55
	s_nop 1
	v_permlane32_swap_b32_e32 v55, v75
	s_and_saveexec_b64 s[0:1], s[42:43]
	v_add_f32_e32 v55, v55, v75
	ds_write_b32 v32, v55 offset:64
	s_or_b64 exec, exec, s[0:1]
	s_waitcnt vmcnt(7)
	v_lshlrev_b32_e32 v112, 16, v106
	v_mul_f32_e32 v55, 0xbfb8aa3b, v112
	v_exp_f32_e32 v55, v55
	v_and_b32_e32 v113, 0xffff0000, v106
	s_waitcnt lgkmcnt(7)
	v_lshlrev_b32_e32 v110, 16, v108
	v_and_b32_e32 v111, 0xffff0000, v108
	v_add_f32_e32 v55, 1.0, v55
	v_rcp_f32_e32 v114, v55
	v_mul_f32_e32 v55, 0xbfb8aa3b, v113
	v_exp_f32_e32 v55, v55
	v_pk_fma_f32 v[38:39], v[70:71], v[110:111], v[38:39]
	v_lshlrev_b32_e32 v108, 16, v109
	v_pk_mul_f32 v[38:39], v[38:39], v[112:113]
	v_add_f32_e32 v55, 1.0, v55
	v_rcp_f32_e32 v115, v55
	v_and_b32_e32 v109, 0xffff0000, v109
	v_pk_fma_f32 v[40:41], v[70:71], v[108:109], v[40:41]
	v_pk_mul_f32 v[38:39], v[38:39], v[114:115]
	s_nop 0
	v_mul_f32_e32 v106, v39, v39
	v_pk_fma_f32 v[110:111], v[38:39], v[38:39], v[106:107] op_sel_hi:[1,1,0]
	v_lshlrev_b32_e32 v106, 16, v107
	v_mul_f32_e32 v55, 0xbfb8aa3b, v106
	v_exp_f32_e32 v55, v55
	v_and_b32_e32 v107, 0xffff0000, v107
	v_pk_mul_f32 v[40:41], v[40:41], v[106:107]
	v_add_f32_e32 v55, 1.0, v55
	v_rcp_f32_e32 v112, v55
	v_mul_f32_e32 v55, 0xbfb8aa3b, v107
	v_exp_f32_e32 v55, v55
	s_nop 0
	v_add_f32_e32 v55, 1.0, v55
	v_rcp_f32_e32 v113, v55
	s_nop 0
	v_pk_mul_f32 v[40:41], v[40:41], v[112:113]
	s_nop 0
	v_pk_fma_f32 v[106:107], v[40:41], v[40:41], v[110:111]
	s_waitcnt vmcnt(6)
	v_lshlrev_b32_e32 v110, 16, v102
	v_mul_f32_e32 v55, 0xbfb8aa3b, v110
	v_exp_f32_e32 v55, v55
	v_and_b32_e32 v111, 0xffff0000, v102
	v_mul_f32_e32 v108, v41, v41
	v_pk_add_f32 v[106:107], v[108:109], v[106:107] op_sel_hi:[0,1]
	v_add_f32_e32 v55, 1.0, v55
	v_rcp_f32_e32 v112, v55
	v_mul_f32_e32 v55, 0xbfb8aa3b, v111
	v_exp_f32_e32 v55, v55
	s_waitcnt lgkmcnt(6)
	v_lshlrev_b32_e32 v108, 16, v104
	v_and_b32_e32 v109, 0xffff0000, v104
	v_pk_fma_f32 v[20:21], v[70:71], v[108:109], v[20:21]
	v_add_f32_e32 v55, 1.0, v55
	v_rcp_f32_e32 v113, v55
	v_pk_mul_f32 v[20:21], v[20:21], v[110:111]
	v_lshlrev_b32_e32 v104, 16, v105
	v_and_b32_e32 v105, 0xffff0000, v105
	v_pk_mul_f32 v[20:21], v[20:21], v[112:113]
	v_pk_fma_f32 v[22:23], v[70:71], v[104:105], v[22:23]
	v_pk_fma_f32 v[106:107], v[20:21], v[20:21], v[106:107]
	v_mul_f32_e32 v102, v21, v21
	v_pk_add_f32 v[106:107], v[102:103], v[106:107] op_sel_hi:[0,1]
	v_lshlrev_b32_e32 v102, 16, v103
	v_mul_f32_e32 v55, 0xbfb8aa3b, v102
	v_exp_f32_e32 v55, v55
	v_and_b32_e32 v103, 0xffff0000, v103
	v_pk_mul_f32 v[22:23], v[22:23], v[102:103]
	v_add_f32_e32 v55, 1.0, v55
	v_rcp_f32_e32 v108, v55
	v_mul_f32_e32 v55, 0xbfb8aa3b, v103
	v_exp_f32_e32 v55, v55
	s_nop 0
	v_add_f32_e32 v55, 1.0, v55
	v_rcp_f32_e32 v109, v55
	s_nop 0
	v_pk_mul_f32 v[22:23], v[22:23], v[108:109]
	s_nop 0
	v_pk_fma_f32 v[102:103], v[22:23], v[22:23], v[106:107]
	s_waitcnt vmcnt(5)
	v_lshlrev_b32_e32 v106, 16, v98
	v_mul_f32_e32 v55, 0xbfb8aa3b, v106
	v_exp_f32_e32 v55, v55
	v_and_b32_e32 v107, 0xffff0000, v98
	v_mul_f32_e32 v104, v23, v23
	v_pk_add_f32 v[102:103], v[104:105], v[102:103] op_sel_hi:[0,1]
	v_add_f32_e32 v55, 1.0, v55
	v_rcp_f32_e32 v108, v55
	v_mul_f32_e32 v55, 0xbfb8aa3b, v107
	v_exp_f32_e32 v55, v55
	s_waitcnt lgkmcnt(5)
	v_lshlrev_b32_e32 v104, 16, v100
	v_and_b32_e32 v105, 0xffff0000, v100
	v_pk_fma_f32 v[16:17], v[70:71], v[104:105], v[16:17]
	v_add_f32_e32 v55, 1.0, v55
	v_rcp_f32_e32 v109, v55
	v_pk_mul_f32 v[16:17], v[16:17], v[106:107]
	v_lshlrev_b32_e32 v100, 16, v101
	v_and_b32_e32 v101, 0xffff0000, v101
	v_pk_mul_f32 v[16:17], v[16:17], v[108:109]
	v_pk_fma_f32 v[18:19], v[70:71], v[100:101], v[18:19]
	v_pk_fma_f32 v[102:103], v[16:17], v[16:17], v[102:103]
	v_mul_f32_e32 v98, v17, v17
	v_pk_add_f32 v[102:103], v[98:99], v[102:103] op_sel_hi:[0,1]
	v_lshlrev_b32_e32 v98, 16, v99
	v_mul_f32_e32 v55, 0xbfb8aa3b, v98
	v_exp_f32_e32 v55, v55
	v_and_b32_e32 v99, 0xffff0000, v99
	v_pk_mul_f32 v[18:19], v[18:19], v[98:99]
	v_add_f32_e32 v55, 1.0, v55
	v_rcp_f32_e32 v104, v55
	v_mul_f32_e32 v55, 0xbfb8aa3b, v99
	v_exp_f32_e32 v55, v55
	s_nop 0
	v_add_f32_e32 v55, 1.0, v55
	v_rcp_f32_e32 v105, v55
	s_nop 0
	v_pk_mul_f32 v[18:19], v[18:19], v[104:105]
	s_nop 0
	v_pk_fma_f32 v[98:99], v[18:19], v[18:19], v[102:103]
	s_waitcnt vmcnt(4)
	v_lshlrev_b32_e32 v102, 16, v94
	v_mul_f32_e32 v55, 0xbfb8aa3b, v102
	v_exp_f32_e32 v55, v55
	v_and_b32_e32 v103, 0xffff0000, v94
	v_mul_f32_e32 v100, v19, v19
	v_pk_add_f32 v[98:99], v[100:101], v[98:99] op_sel_hi:[0,1]
	v_add_f32_e32 v55, 1.0, v55
	v_rcp_f32_e32 v104, v55
	v_mul_f32_e32 v55, 0xbfb8aa3b, v103
	v_exp_f32_e32 v55, v55
	s_waitcnt lgkmcnt(4)
	v_lshlrev_b32_e32 v100, 16, v96
	v_and_b32_e32 v101, 0xffff0000, v96
	v_pk_fma_f32 v[24:25], v[70:71], v[100:101], v[24:25]
	v_add_f32_e32 v55, 1.0, v55
	v_rcp_f32_e32 v105, v55
	v_pk_mul_f32 v[24:25], v[24:25], v[102:103]
	v_lshlrev_b32_e32 v96, 16, v97
	v_and_b32_e32 v97, 0xffff0000, v97
	v_pk_mul_f32 v[24:25], v[24:25], v[104:105]
	v_pk_fma_f32 v[26:27], v[70:71], v[96:97], v[26:27]
	v_pk_fma_f32 v[98:99], v[24:25], v[24:25], v[98:99]
	v_mul_f32_e32 v94, v25, v25
	v_pk_add_f32 v[98:99], v[94:95], v[98:99] op_sel_hi:[0,1]
	v_lshlrev_b32_e32 v94, 16, v95
	v_mul_f32_e32 v55, 0xbfb8aa3b, v94
	v_exp_f32_e32 v55, v55
	v_and_b32_e32 v95, 0xffff0000, v95
	v_pk_mul_f32 v[26:27], v[26:27], v[94:95]
	v_add_f32_e32 v55, 1.0, v55
	v_rcp_f32_e32 v100, v55
	v_mul_f32_e32 v55, 0xbfb8aa3b, v95
	v_exp_f32_e32 v55, v55
	s_nop 0
	v_add_f32_e32 v55, 1.0, v55
	v_rcp_f32_e32 v101, v55
	s_nop 0
	v_pk_mul_f32 v[26:27], v[26:27], v[100:101]
	s_nop 0
	v_pk_fma_f32 v[94:95], v[26:27], v[26:27], v[98:99]
	v_mul_f32_e32 v96, v27, v27
	v_pk_add_f32 v[94:95], v[96:97], v[94:95] op_sel_hi:[0,1]
	v_mov_b32_e32 v55, v94
	s_nop 1
	v_permlane16_swap_b32_e32 v94, v55
	v_add_f32_e32 v55, v94, v55
	v_mov_b32_e32 v75, v55
	s_nop 1
	v_permlane32_swap_b32_e32 v55, v75
	s_and_saveexec_b64 s[0:1], s[42:43]
	v_add_f32_e32 v55, v55, v75
	ds_write_b32 v32, v55 offset:128
	s_or_b64 exec, exec, s[0:1]
	s_waitcnt vmcnt(3)
	v_lshlrev_b32_e32 v96, 16, v90
	v_mul_f32_e32 v55, 0xbfb8aa3b, v96
	v_exp_f32_e32 v55, v55
	v_and_b32_e32 v97, 0xffff0000, v90
	v_lshlrev_b32_e32 v90, 16, v91
	s_waitcnt lgkmcnt(3)
	v_lshlrev_b32_e32 v94, 16, v92
	v_add_f32_e32 v55, 1.0, v55
	v_rcp_f32_e32 v98, v55
	v_mul_f32_e32 v55, 0xbfb8aa3b, v97
	v_exp_f32_e32 v55, v55
	v_and_b32_e32 v95, 0xffff0000, v92
	v_pk_fma_f32 v[12:13], v[70:71], v[94:95], v[12:13]
	v_and_b32_e32 v91, 0xffff0000, v91
	v_add_f32_e32 v55, 1.0, v55
	v_rcp_f32_e32 v99, v55
	v_mul_f32_e32 v55, 0xbfb8aa3b, v90
	v_exp_f32_e32 v55, v55
	v_pk_mul_f32 v[12:13], v[12:13], v[96:97]
	v_lshlrev_b32_e32 v92, 16, v93
	v_and_b32_e32 v93, 0xffff0000, v93
	v_add_f32_e32 v55, 1.0, v55
	v_rcp_f32_e32 v96, v55
	v_mul_f32_e32 v55, 0xbfb8aa3b, v91
	v_exp_f32_e32 v55, v55
	v_pk_mul_f32 v[94:95], v[12:13], v[98:99]
	v_pk_fma_f32 v[14:15], v[70:71], v[92:93], v[14:15]
	v_mul_f32_e32 v12, v95, v95
	v_add_f32_e32 v55, 1.0, v55
	v_rcp_f32_e32 v97, v55
	v_pk_mul_f32 v[14:15], v[14:15], v[90:91]
	v_pk_fma_f32 v[12:13], v[94:95], v[94:95], v[12:13] op_sel_hi:[1,1,0]
	s_waitcnt vmcnt(2)
	v_lshlrev_b32_e32 v92, 16, v86
	v_pk_mul_f32 v[90:91], v[14:15], v[96:97]
	v_and_b32_e32 v93, 0xffff0000, v86
	v_pk_fma_f32 v[12:13], v[90:91], v[90:91], v[12:13]
	v_mul_f32_e32 v14, v91, v91
	v_pk_add_f32 v[12:13], v[14:15], v[12:13] op_sel_hi:[0,1]
	s_waitcnt lgkmcnt(2)
	v_lshlrev_b32_e32 v14, 16, v88
	v_and_b32_e32 v15, 0xffff0000, v88
	v_mul_f32_e32 v55, 0xbfb8aa3b, v92
	v_pk_fma_f32 v[4:5], v[70:71], v[14:15], v[4:5]
	v_mul_f32_e32 v14, 0xbfb8aa3b, v93
	v_exp_f32_e32 v55, v55
	v_exp_f32_e32 v14, v14
	v_pk_mul_f32 v[4:5], v[4:5], v[92:93]
	v_and_b32_e32 v15, 0xffff0000, v87
	v_add_f32_e32 v55, 1.0, v55
	v_add_f32_e32 v14, 1.0, v14
	v_rcp_f32_e32 v96, v55
	v_rcp_f32_e32 v97, v14
	v_lshlrev_b32_e32 v14, 16, v87
	v_mul_f32_e32 v55, 0xbfb8aa3b, v14
	v_exp_f32_e32 v55, v55
	v_pk_mul_f32 v[92:93], v[4:5], v[96:97]
	v_add_f32_e32 v55, 1.0, v55
	v_pk_fma_f32 v[4:5], v[92:93], v[92:93], v[12:13]
	v_mul_f32_e32 v12, v93, v93
	v_pk_add_f32 v[4:5], v[12:13], v[4:5] op_sel_hi:[0,1]
	v_lshlrev_b32_e32 v12, 16, v89
	v_and_b32_e32 v13, 0xffff0000, v89
	v_pk_fma_f32 v[6:7], v[70:71], v[12:13], v[6:7]
	v_mul_f32_e32 v12, 0xbfb8aa3b, v15
	v_exp_f32_e32 v12, v12
	v_rcp_f32_e32 v86, v55
	v_pk_mul_f32 v[6:7], v[6:7], v[14:15]
	s_waitcnt vmcnt(1)
	v_and_b32_e32 v13, 0xffff0000, v82
	v_add_f32_e32 v12, 1.0, v12
	v_rcp_f32_e32 v87, v12
	v_lshlrev_b32_e32 v12, 16, v82
	v_mul_f32_e32 v14, 0xbfb8aa3b, v12
	v_exp_f32_e32 v14, v14
	v_pk_mul_f32 v[86:87], v[6:7], v[86:87]
	v_add_f32_e32 v14, 1.0, v14
	v_pk_fma_f32 v[4:5], v[86:87], v[86:87], v[4:5]
	v_mul_f32_e32 v6, v87, v87
	v_pk_add_f32 v[4:5], v[6:7], v[4:5] op_sel_hi:[0,1]
	s_waitcnt lgkmcnt(1)
	v_lshlrev_b32_e32 v6, 16, v84
	v_and_b32_e32 v7, 0xffff0000, v84
	v_pk_fma_f32 v[0:1], v[70:71], v[6:7], v[0:1]
	v_mul_f32_e32 v6, 0xbfb8aa3b, v13
	v_exp_f32_e32 v6, v6
	v_rcp_f32_e32 v14, v14
	v_pk_mul_f32 v[0:1], v[0:1], v[12:13]
	v_and_b32_e32 v7, 0xffff0000, v83
	v_add_f32_e32 v6, 1.0, v6
	v_rcp_f32_e32 v15, v6
	v_lshlrev_b32_e32 v6, 16, v83
	v_mul_f32_e32 v12, 0xbfb8aa3b, v6
	v_exp_f32_e32 v12, v12
	v_pk_mul_f32 v[88:89], v[0:1], v[14:15]
	v_add_f32_e32 v12, 1.0, v12
	v_pk_fma_f32 v[0:1], v[88:89], v[88:89], v[4:5]
	v_mul_f32_e32 v4, v89, v89
	v_pk_add_f32 v[0:1], v[4:5], v[0:1] op_sel_hi:[0,1]
	v_lshlrev_b32_e32 v4, 16, v85
	v_and_b32_e32 v5, 0xffff0000, v85
	v_pk_fma_f32 v[2:3], v[70:71], v[4:5], v[2:3]
	v_mul_f32_e32 v4, 0xbfb8aa3b, v7
	v_exp_f32_e32 v4, v4
	v_rcp_f32_e32 v12, v12
	v_pk_mul_f32 v[2:3], v[2:3], v[6:7]
	s_waitcnt vmcnt(0)
	v_and_b32_e32 v5, 0xffff0000, v78
	v_add_f32_e32 v4, 1.0, v4
	v_rcp_f32_e32 v13, v4
	v_lshlrev_b32_e32 v4, 16, v78
	v_mul_f32_e32 v6, 0xbfb8aa3b, v4
	v_exp_f32_e32 v6, v6
	v_pk_mul_f32 v[82:83], v[2:3], v[12:13]
	v_add_f32_e32 v6, 1.0, v6
	v_pk_fma_f32 v[0:1], v[82:83], v[82:83], v[0:1]
	v_mul_f32_e32 v2, v83, v83
	v_pk_add_f32 v[0:1], v[2:3], v[0:1] op_sel_hi:[0,1]
	s_waitcnt lgkmcnt(0)
	v_lshlrev_b32_e32 v2, 16, v80
	v_and_b32_e32 v3, 0xffff0000, v80
	v_pk_fma_f32 v[2:3], v[70:71], v[2:3], v[8:9]
	v_rcp_f32_e32 v6, v6
	v_pk_mul_f32 v[2:3], v[2:3], v[4:5]
	v_mul_f32_e32 v4, 0xbfb8aa3b, v5
	v_exp_f32_e32 v4, v4
	v_and_b32_e32 v5, 0xffff0000, v79
	v_add_f32_e32 v4, 1.0, v4
	v_rcp_f32_e32 v7, v4
	v_lshlrev_b32_e32 v4, 16, v79
	v_pk_mul_f32 v[84:85], v[2:3], v[6:7]
	s_nop 0
	v_pk_fma_f32 v[0:1], v[84:85], v[84:85], v[0:1]
	v_mul_f32_e32 v2, v85, v85
	v_pk_add_f32 v[0:1], v[2:3], v[0:1] op_sel_hi:[0,1]
	v_lshlrev_b32_e32 v2, 16, v81
	v_and_b32_e32 v3, 0xffff0000, v81
	v_pk_fma_f32 v[2:3], v[70:71], v[2:3], v[10:11]
	v_mul_f32_e32 v6, 0xbfb8aa3b, v4
	v_pk_mul_f32 v[2:3], v[2:3], v[4:5]
	v_mul_f32_e32 v4, 0xbfb8aa3b, v5
	v_exp_f32_e32 v6, v6
	v_exp_f32_e32 v4, v4
	v_add_f32_e32 v6, 1.0, v6
	v_add_f32_e32 v4, 1.0, v4
	v_rcp_f32_e32 v6, v6
	v_rcp_f32_e32 v7, v4
	s_nop 0
	v_pk_mul_f32 v[70:71], v[2:3], v[6:7]
	s_nop 0
	v_pk_fma_f32 v[0:1], v[70:71], v[70:71], v[0:1]
	v_mul_f32_e32 v2, v71, v71
	v_pk_add_f32 v[0:1], v[2:3], v[0:1] op_sel_hi:[0,1]
	v_mov_b32_e32 v1, v0
	s_nop 1
	v_permlane16_swap_b32_e32 v0, v1
	v_add_f32_e32 v0, v0, v1
	v_mov_b32_e32 v1, v0
	s_nop 1
	v_permlane32_swap_b32_e32 v0, v1
	s_and_saveexec_b64 s[0:1], s[42:43]
	s_cbranch_execz .LBB0_1237
	v_add_f32_e32 v0, v0, v1
	ds_write_b32 v32, v0 offset:192
	s_branch .LBB0_1237

.LBB0_1268:
	s_and_b32 s19, s27, 7
	s_lshl_b32 s0, s19, 3
	s_add_i32 s20, s0, s22
	s_lshl_b32 s12, s20, 6
	s_ashr_i32 s18, s27, 3
	s_ashr_i32 s13, s12, 31
	s_lshl_b32 s28, s18, 6
	s_lshl_b64 s[14:15], s[12:13], 1
	s_waitcnt vmcnt(8)
	v_or_b32_e32 v30, s28, v171
	v_lshl_add_u64 v[28:29], v[160:161], 0, s[14:15]
	v_mad_i64_i32 v[0:1], s[0:1], v30, s77, v[28:29]
	v_or_b32_e32 v4, 8, v30
	global_load_dwordx4 v[0:3], v[0:1], off
	v_mad_i64_i32 v[4:5], s[0:1], v4, s77, v[28:29]
	v_or_b32_e32 v8, 16, v30
	global_load_dwordx4 v[4:7], v[4:5], off
	v_mad_i64_i32 v[8:9], s[0:1], v8, s77, v[28:29]
	v_or_b32_e32 v12, 24, v30
	global_load_dwordx4 v[8:11], v[8:9], off
	v_mad_i64_i32 v[12:13], s[0:1], v12, s77, v[28:29]
	v_or_b32_e32 v16, 32, v30
	global_load_dwordx4 v[12:15], v[12:13], off
	v_mad_i64_i32 v[16:17], s[0:1], v16, s77, v[28:29]
	v_or_b32_e32 v20, 40, v30
	global_load_dwordx4 v[16:19], v[16:17], off
	v_mad_i64_i32 v[20:21], s[0:1], v20, s77, v[28:29]
	v_or_b32_e32 v24, 48, v30
	global_load_dwordx4 v[20:23], v[20:21], off
	v_mad_i64_i32 v[24:25], s[0:1], v24, s77, v[28:29]
	v_or_b32_e32 v30, 56, v30
	global_load_dwordx4 v[24:27], v[24:25], off
	v_mad_i64_i32 v[28:29], s[0:1], v30, s77, v[28:29]
	global_load_dwordx4 v[28:31], v[28:29], off
	s_lshl_b32 s0, s18, 6
	s_add_i32 s0, s0, s20
	s_lshl_b32 s0, s0, 9
	v_lshl_add_u32 v198, v169, 3, s0
	v_mov_b32_e32 v199, 0
	v_lshl_add_u64 v[198:199], s[24:25], 0, v[198:199]
	s_mov_b64 s[0:1], 0x400000
	s_nop 0
	v_lshl_add_u64 v[198:199], v[198:199], 0, s[0:1]
	global_load_dwordx2 v[198:199], v[198:199], off
	s_ashr_i32 s21, s20, 31
	v_readlane_b32 s56, v251, 32
	s_lshl_b64 s[16:17], s[20:21], 2
	v_readlane_b32 s58, v251, 34
	v_readlane_b32 s59, v251, 35
	s_add_u32 s0, s58, s16
	s_addc_u32 s1, s59, s17
	v_readlane_b32 s60, v251, 36
	v_readlane_b32 s61, v251, 37
	v_or_b32_e32 v172, s28, v166
	v_lshlrev_b32_e32 v32, 1, v158
	s_movk_i32 s74, 0x2000
	s_movk_i32 s76, 0x1000
	v_readlane_b32 s62, v251, 38
	v_readlane_b32 s63, v251, 39
	v_readlane_b32 s57, v251, 33
	v_readlane_b32 s64, v251, 40
	v_readlane_b32 s65, v251, 41
	v_readlane_b32 s66, v251, 42
	v_readlane_b32 s67, v251, 43
	v_readlane_b32 s68, v251, 44
	v_readlane_b32 s69, v251, 45
	v_readlane_b32 s70, v251, 46
	v_readlane_b32 s71, v251, 47
	s_waitcnt vmcnt(8)
	ds_write_b128 v212, v[0:3]
	s_waitcnt vmcnt(7)
	ds_write_b128 v212, v[4:7] offset:1280
	s_waitcnt vmcnt(6)
	ds_write_b128 v212, v[8:11] offset:2560
	s_waitcnt vmcnt(5)
	ds_write_b128 v212, v[12:15] offset:3840
	s_waitcnt vmcnt(4)
	ds_write_b128 v212, v[16:19] offset:5120
	s_waitcnt vmcnt(3)
	ds_write_b128 v212, v[20:23] offset:6400
	s_waitcnt vmcnt(2)
	ds_write_b128 v212, v[24:27] offset:7680
	s_waitcnt vmcnt(1)
	ds_write_b128 v212, v[28:31] offset:8960
	s_lshl_b32 s86, s19, 8
	s_ashr_i32 s19, s18, 31
	s_waitcnt vmcnt(0)
	ds_write_b32 v183, v198
	ds_write_b32 v184, v199
	v_mov_b64_e32 v[0:1], s[8:9]
	v_mad_i64_i32 v[0:1], s[0:1], v172, s77, v[0:1]
	v_lshl_add_u64 v[0:1], v[0:1], 0, s[86:87]
	v_lshl_add_u64 v[8:9], v[0:1], 0, v[32:33]
	s_mov_b64 s[0:1], 0x2800
	v_lshl_add_u64 v[74:75], v[8:9], 0, s[0:1]
	v_add_co_u32_e64 v0, s[0:1], s74, v8
	s_movk_i32 s77, 0x3000
	s_nop 0
	v_addc_co_u32_e64 v1, s[0:1], 0, v9, s[0:1]
	s_mov_b32 s0, 0x32000
	s_nop 0
	v_add_co_u32_e64 v30, s[0:1], s0, v8
	global_load_dwordx4 v[4:7], v[0:1], off offset:2048
	s_nop 0
	global_load_dwordx4 v[0:3], v[74:75], off offset:64
	global_load_dwordx4 v[70:73], v[74:75], off offset:128
	global_load_dwordx4 v[66:69], v[74:75], off offset:192
	v_addc_co_u32_e64 v31, s[0:1], 0, v9, s[0:1]
	s_mov_b32 s0, 0x62000
	s_nop 0
	v_add_co_u32_e64 v88, s[0:1], s0, v8
	global_load_dwordx4 v[62:65], v[30:31], off offset:2048
	global_load_dwordx4 v[58:61], v[30:31], off offset:2112
	global_load_dwordx4 v[54:57], v[30:31], off offset:2176
	global_load_dwordx4 v[50:53], v[30:31], off offset:2240
	v_addc_co_u32_e64 v89, s[0:1], 0, v9, s[0:1]
	s_mov_b32 s0, 0x92000
	s_nop 0
	v_add_co_u32_e64 v86, s[0:1], s0, v8
	global_load_dwordx4 v[46:49], v[88:89], off offset:2048
	global_load_dwordx4 v[42:45], v[88:89], off offset:2112
	global_load_dwordx4 v[38:41], v[88:89], off offset:2176
	global_load_dwordx4 v[24:27], v[88:89], off offset:2240
	v_addc_co_u32_e64 v87, s[0:1], 0, v9, s[0:1]
	global_load_dwordx4 v[20:23], v[86:87], off offset:2048
	global_load_dwordx4 v[16:19], v[86:87], off offset:2112
	global_load_dwordx4 v[8:11], v[86:87], off offset:2176
	global_load_dwordx4 v[12:15], v[86:87], off offset:2240
	s_waitcnt lgkmcnt(0)
	ds_read2_b32 v[102:103], v185 offset1:16
	ds_read2_b32 v[28:29], v185 offset0:32 offset1:48
	global_load_dwordx4 v[82:85], v[74:75], off offset:-2048
	global_load_dwordx4 v[92:95], v[74:75], off offset:-1984
	global_load_dwordx4 v[96:99], v[74:75], off offset:-1920
	global_load_dwordx4 v[104:107], v[74:75], off offset:-1856
	s_waitcnt vmcnt(3)
	v_mfma_f32_16x16x32_bf16 v[74:77], v[82:85], v[4:7], 0
	ds_read_b64 v[100:101], v186
	ds_read_b32 v32, v188
	ds_read_b32 v90, v189
	ds_read_b32 v118, v190
	ds_read_b32 v91, v191
	s_mov_b32 s0, 0x5040100
	s_waitcnt vmcnt(2)
	v_mfma_f32_16x16x32_bf16 v[74:77], v[92:95], v[0:3], v[74:77]
	s_waitcnt vmcnt(1)
	v_mfma_f32_16x16x32_bf16 v[74:77], v[96:99], v[70:73], v[74:77]
	v_mfma_f32_16x16x32_bf16 v[108:111], v[82:85], v[62:65], 0
	s_waitcnt vmcnt(0)
	v_mfma_f32_16x16x32_bf16 v[78:81], v[104:107], v[66:69], v[74:77]
	s_waitcnt lgkmcnt(4)
	s_nop 3
	v_sub_f32_e32 v76, v103, v100
	v_min_f32_e32 v76, 0, v76
	v_mfma_f32_16x16x32_bf16 v[108:111], v[92:95], v[58:61], v[108:111]
	v_mul_f32_e32 v76, 0x3fb8aa3b, v76
	v_exp_f32_e32 v114, v76
	v_sub_f32_e32 v76, v103, v101
	v_min_f32_e32 v76, 0, v76
	v_mul_f32_e32 v76, 0x3fb8aa3b, v76
	v_mfma_f32_16x16x32_bf16 v[108:111], v[96:99], v[54:57], v[108:111]
	v_exp_f32_e32 v115, v76
	s_waitcnt lgkmcnt(3)
	v_sub_f32_e32 v76, v103, v32
	s_waitcnt lgkmcnt(1)
	v_sub_f32_e32 v77, v103, v118
	v_min_f32_e32 v76, 0, v76
	v_min_f32_e32 v77, 0, v77
	v_mul_f32_e32 v76, 0x3fb8aa3b, v76
	v_mul_f32_e32 v77, 0x3fb8aa3b, v77
	v_exp_f32_e32 v76, v76
	v_exp_f32_e32 v77, v77
	v_mfma_f32_16x16x32_bf16 v[108:111], v[104:107], v[50:53], v[108:111]
	v_sub_f32_e32 v74, v102, v100
	v_min_f32_e32 v74, 0, v74
	v_mul_f32_e32 v74, 0x3fb8aa3b, v74
	s_waitcnt lgkmcnt(0)
	v_pk_mul_f32 v[76:77], v[90:91], v[76:77]
	v_exp_f32_e32 v119, v74
	v_sub_f32_e32 v74, v102, v101
	s_nop 0
	v_pk_mul_f32 v[76:77], v[76:77], v[110:111]
	v_mfma_f32_16x16x32_bf16 v[110:113], v[82:85], v[46:49], 0
	v_min_f32_e32 v74, 0, v74
	v_mul_f32_e32 v74, 0x3fb8aa3b, v74
	v_exp_f32_e32 v120, v74
	v_mfma_f32_16x16x32_bf16 v[82:85], v[82:85], v[20:23], 0
	v_sub_f32_e32 v74, v102, v32
	v_sub_f32_e32 v75, v102, v118
	v_min_f32_e32 v74, 0, v74
	v_min_f32_e32 v75, 0, v75
	v_mfma_f32_16x16x32_bf16 v[82:85], v[92:95], v[16:19], v[82:85]
	v_mul_f32_e32 v74, 0x3fb8aa3b, v74
	v_mul_f32_e32 v75, 0x3fb8aa3b, v75
	v_exp_f32_e32 v74, v74
	v_exp_f32_e32 v75, v75
	v_mfma_f32_16x16x32_bf16 v[82:85], v[96:99], v[8:11], v[82:85]
	v_mul_f32_e64 v74, v90, v74
	v_mul_f32_e64 v75, v91, v75
	v_mfma_f32_16x16x32_bf16 v[110:113], v[92:95], v[42:45], v[110:113]
	v_mul_f32_e64 v74, v74, v80
	v_mul_f32_e64 v75, v75, v81
	v_sub_f32_e32 v80, v28, v100
	v_min_f32_e32 v80, 0, v80
	v_mfma_f32_16x16x32_bf16 v[92:95], v[104:107], v[12:15], v[82:85]
	v_mul_f32_e32 v80, 0x3fb8aa3b, v80
	v_exp_f32_e32 v116, v80
	v_sub_f32_e32 v80, v28, v101
	v_sub_f32_e32 v82, v29, v100
	v_sub_f32_e32 v83, v29, v101
	v_min_f32_e32 v82, 0, v82
	v_min_f32_e32 v83, 0, v83
	v_mfma_f32_16x16x32_bf16 v[110:113], v[96:99], v[38:41], v[110:113]
	v_mul_f32_e32 v82, 0x3fb8aa3b, v82
	v_mul_f32_e32 v83, 0x3fb8aa3b, v83
	ds_read_b64 v[96:97], v187
	v_min_f32_e32 v80, 0, v80
	v_exp_f32_e32 v82, v82
	v_exp_f32_e32 v83, v83
	v_mul_f32_e32 v80, 0x3fb8aa3b, v80
	v_exp_f32_e32 v117, v80
	v_sub_f32_e32 v80, v28, v32
	v_sub_f32_e32 v32, v29, v32
	v_min_f32_e32 v32, 0, v32
	s_waitcnt lgkmcnt(0)
	v_pk_mul_f32 v[82:83], v[96:97], v[82:83]
	v_mul_f32_e32 v32, 0x3fb8aa3b, v32
	v_sub_f32_e32 v81, v28, v118
	v_pk_mul_f32 v[82:83], v[82:83], v[92:93]
	v_exp_f32_e32 v92, v32
	v_sub_f32_e32 v32, v29, v118
	v_min_f32_e32 v80, 0, v80
	v_min_f32_e32 v81, 0, v81
	v_min_f32_e32 v32, 0, v32
	v_mul_f32_e32 v80, 0x3fb8aa3b, v80
	v_mul_f32_e32 v81, 0x3fb8aa3b, v81
	v_mul_f32_e32 v84, v96, v119
	v_mul_f32_e32 v32, 0x3fb8aa3b, v32
	v_exp_f32_e32 v80, v80
	v_exp_f32_e32 v81, v81
	v_mul_f32_e32 v78, v84, v78
	v_exp_f32_e32 v93, v32
	v_mfma_f32_16x16x32_bf16 v[110:113], v[104:107], v[24:27], v[110:113]
	v_cndmask_b32_e64 v126, v78, 0, s[46:47]
	v_mul_f32_e32 v78, v97, v120
	v_mul_f32_e32 v78, v78, v79
	v_cndmask_b32_e64 v127, 0, v78, s[48:49]
	v_pk_mul_f32 v[78:79], v[96:97], v[114:115]
	v_pk_mul_f32 v[80:81], v[90:91], v[80:81]
	v_pk_mul_f32 v[84:85], v[78:79], v[108:109]
	v_pk_mul_f32 v[78:79], v[96:97], v[116:117]
	v_pk_mul_f32 v[90:91], v[90:91], v[92:93]
	v_pk_mul_f32 v[78:79], v[78:79], v[110:111]
	v_pk_mul_f32 v[90:91], v[90:91], v[94:95]
	global_load_dwordx4 v[92:95], v[30:31], off
	global_load_dwordx4 v[96:99], v[30:31], off offset:64
	global_load_dwordx4 v[104:107], v[30:31], off offset:128
	global_load_dwordx4 v[108:111], v[30:31], off offset:192
	v_pk_mul_f32 v[80:81], v[80:81], v[112:113]
	ds_read_b128 v[112:115], v186 offset:64
	s_waitcnt vmcnt(3)
	v_mfma_f32_16x16x32_bf16 v[116:119], v[92:95], v[62:65], 0
	s_waitcnt lgkmcnt(0)
	v_sub_f32_e32 v30, v103, v112
	v_min_f32_e32 v30, 0, v30
	v_mul_f32_e32 v30, 0x3fb8aa3b, v30
	v_mfma_f32_16x16x32_bf16 v[120:123], v[92:95], v[46:49], 0
	v_exp_f32_e32 v32, v30
	v_sub_f32_e32 v30, v103, v113
	v_min_f32_e32 v30, 0, v30
	v_mfma_f32_16x16x32_bf16 v[92:95], v[92:95], v[20:23], 0
	v_mul_f32_e32 v30, 0x3fb8aa3b, v30
	v_exp_f32_e32 v128, v30
	v_sub_f32_e32 v100, v28, v112
	s_waitcnt vmcnt(2)
	v_mfma_f32_16x16x32_bf16 v[116:119], v[96:99], v[58:61], v[116:119]
	v_sub_f32_e32 v101, v28, v113
	v_min_f32_e32 v100, 0, v100
	v_min_f32_e32 v101, 0, v101
	v_mfma_f32_16x16x32_bf16 v[120:123], v[96:99], v[42:45], v[120:123]
	v_mul_f32_e32 v100, 0x3fb8aa3b, v100
	v_mul_f32_e32 v101, 0x3fb8aa3b, v101
	v_exp_f32_e32 v100, v100
	v_mfma_f32_16x16x32_bf16 v[92:95], v[96:99], v[16:19], v[92:95]
	v_sub_f32_e32 v96, v29, v112
	v_min_f32_e32 v96, 0, v96
	v_mul_f32_e32 v96, 0x3fb8aa3b, v96
	s_waitcnt vmcnt(1)
	v_mfma_f32_16x16x32_bf16 v[116:119], v[104:107], v[54:57], v[116:119]
	v_exp_f32_e32 v101, v101
	v_sub_f32_e32 v30, v103, v114
	v_sub_f32_e32 v31, v103, v115
	v_mfma_f32_16x16x32_bf16 v[120:123], v[104:107], v[38:41], v[120:123]
	v_min_f32_e32 v30, 0, v30
	v_min_f32_e32 v31, 0, v31
	v_sub_f32_e32 v124, v28, v114
	v_mfma_f32_16x16x32_bf16 v[92:95], v[104:107], v[8:11], v[92:95]
	v_exp_f32_e32 v104, v96
	v_sub_f32_e32 v96, v29, v113
	v_min_f32_e32 v96, 0, v96
	v_mul_f32_e32 v96, 0x3fb8aa3b, v96
	v_exp_f32_e32 v105, v96
	ds_read_b128 v[96:99], v187 offset:64
	s_waitcnt vmcnt(0)
	v_mfma_f32_16x16x32_bf16 v[116:119], v[108:111], v[50:53], v[116:119]
	v_sub_f32_e32 v125, v28, v115
	v_mul_f32_e32 v30, 0x3fb8aa3b, v30
	v_mul_f32_e32 v31, 0x3fb8aa3b, v31
	s_waitcnt lgkmcnt(0)
	v_mul_f32_e32 v32, v96, v32
	v_mfma_f32_16x16x32_bf16 v[120:123], v[108:111], v[24:27], v[120:123]
	s_nop 1
	v_mul_f32_e32 v32, v32, v116
	v_pk_mul_f32 v[100:101], v[96:97], v[100:101]
	v_min_f32_e32 v124, 0, v124
	v_mfma_f32_16x16x32_bf16 v[92:95], v[108:111], v[12:15], v[92:95]
	v_cndmask_b32_e64 v108, v32, 0, s[46:47]
	v_mul_f32_e32 v32, v97, v128
	v_mul_f32_e32 v32, v32, v117
	v_cndmask_b32_e64 v109, 0, v32, s[48:49]
	v_sub_f32_e32 v32, v29, v114
	v_min_f32_e32 v32, 0, v32
	v_pk_mul_f32 v[96:97], v[96:97], v[104:105]
	v_mul_f32_e32 v32, 0x3fb8aa3b, v32
	v_min_f32_e32 v125, 0, v125
	v_pk_mul_f32 v[92:93], v[96:97], v[92:93]
	v_exp_f32_e32 v96, v32
	v_sub_f32_e32 v32, v29, v115
	v_exp_f32_e32 v30, v30
	v_exp_f32_e32 v31, v31
	v_mul_f32_e32 v124, 0x3fb8aa3b, v124
	v_mul_f32_e32 v125, 0x3fb8aa3b, v125
	v_min_f32_e32 v32, 0, v32
	v_exp_f32_e32 v124, v124
	v_exp_f32_e32 v125, v125
	v_mul_f32_e32 v32, 0x3fb8aa3b, v32
	v_exp_f32_e32 v97, v32
	v_pk_mul_f32 v[30:31], v[98:99], v[30:31]
	v_pk_mul_f32 v[100:101], v[100:101], v[120:121]
	v_pk_mul_f32 v[104:105], v[30:31], v[118:119]
	v_pk_mul_f32 v[30:31], v[98:99], v[124:125]
	v_cvt_pk_bf16_f32 v78, v78, v79
	v_pk_mul_f32 v[106:107], v[30:31], v[122:123]
	v_pk_mul_f32 v[30:31], v[98:99], v[96:97]
	v_cvt_pk_bf16_f32 v79, v80, v81
	v_pk_mul_f32 v[94:95], v[30:31], v[94:95]
	v_cvt_pk_bf16_f32 v31, v74, v75
	v_cvt_pk_bf16_f32 v75, v76, v77
	v_cvt_pk_bf16_f32 v77, v104, v105
	v_cvt_pk_bf16_f32 v74, v84, v85
	v_cndmask_b32_e64 v84, v77, 0, s[52:53]
	v_lshrrev_b32_e32 v77, 16, v77
	v_cndmask_b32_e64 v77, v77, 0, s[50:51]
	v_perm_b32 v77, v77, v84, s0
	v_cvt_pk_bf16_f32 v80, v100, v101
	v_cvt_pk_bf16_f32 v81, v106, v107
	v_cvt_pk_bf16_f32 v82, v82, v83
	v_cvt_pk_bf16_f32 v83, v90, v91
	v_cvt_pk_bf16_f32 v84, v92, v93
	v_cvt_pk_bf16_f32 v85, v94, v95
	global_load_dwordx4 v[90:93], v[88:89], off
	global_load_dwordx4 v[94:97], v[88:89], off offset:64
	global_load_dwordx4 v[98:101], v[88:89], off offset:128
	global_load_dwordx4 v[104:107], v[88:89], off offset:192
	v_cvt_pk_bf16_f32 v76, v108, v109
	ds_read_b128 v[108:111], v186 offset:128
	s_waitcnt vmcnt(3)
	v_mfma_f32_16x16x32_bf16 v[112:115], v[90:93], v[46:49], 0
	s_waitcnt lgkmcnt(0)
	v_sub_f32_e32 v88, v28, v108
	v_min_f32_e32 v88, 0, v88
	v_mul_f32_e32 v88, 0x3fb8aa3b, v88
	v_exp_f32_e32 v118, v88
	v_sub_f32_e32 v88, v28, v109
	v_min_f32_e32 v88, 0, v88
	v_mul_f32_e32 v88, 0x3fb8aa3b, v88
	v_exp_f32_e32 v119, v88
	v_sub_f32_e32 v88, v28, v110
	v_min_f32_e32 v88, 0, v88
	v_mul_f32_e32 v88, 0x3fb8aa3b, v88
	v_exp_f32_e32 v116, v88
	v_sub_f32_e32 v88, v28, v111
	v_min_f32_e32 v88, 0, v88
	v_mul_f32_e32 v88, 0x3fb8aa3b, v88
	v_exp_f32_e32 v117, v88
	v_mfma_f32_16x16x32_bf16 v[88:91], v[90:93], v[20:23], 0
	v_cndmask_b32_e64 v32, v31, 0, s[52:53]
	v_lshrrev_b32_e32 v31, 16, v31
	v_cndmask_b32_e64 v31, v31, 0, s[50:51]
	s_waitcnt vmcnt(2)
	v_mfma_f32_16x16x32_bf16 v[88:91], v[94:97], v[16:19], v[88:91]
	v_perm_b32 v31, v31, v32, s0
	v_cvt_pk_bf16_f32 v30, v126, v127
	v_mul_f32_e32 v28, 0x3fb8aa3b, v28
	s_waitcnt vmcnt(1)
	v_mfma_f32_16x16x32_bf16 v[88:91], v[98:101], v[8:11], v[88:91]
	v_exp_f32_e32 v176, v28
	v_mul_f32_e32 v28, 0x3fb8aa3b, v29
	v_exp_f32_e32 v28, v28
	s_waitcnt vmcnt(0)
	v_mfma_f32_16x16x32_bf16 v[90:93], v[104:107], v[12:15], v[88:91]
	v_mov_b32_e32 v32, v33
	s_nop 1
	v_sub_f32_e32 v88, v29, v108
	v_sub_f32_e32 v89, v29, v109
	v_mfma_f32_16x16x32_bf16 v[112:115], v[94:97], v[42:45], v[112:115]
	v_min_f32_e32 v88, 0, v88
	v_min_f32_e32 v89, 0, v89
	v_mul_f32_e32 v88, 0x3fb8aa3b, v88
	v_mul_f32_e32 v89, 0x3fb8aa3b, v89
	ds_read_b128 v[94:97], v187 offset:128
	v_exp_f32_e32 v88, v88
	v_exp_f32_e32 v89, v89
	v_mfma_f32_16x16x32_bf16 v[112:115], v[98:101], v[38:41], v[112:115]
	s_waitcnt lgkmcnt(0)
	v_mul_f32_e32 v98, v94, v118
	v_pk_mul_f32 v[88:89], v[94:95], v[88:89]
	v_mfma_f32_16x16x32_bf16 v[112:115], v[104:107], v[24:27], v[112:115]
	v_mul_f32_e64 v90, v88, v90
	v_mul_f32_e64 v91, v89, v91
	v_sub_f32_e32 v88, v29, v110
	v_min_f32_e32 v88, 0, v88
	v_mul_f32_e32 v88, 0x3fb8aa3b, v88
	v_exp_f32_e32 v94, v88
	v_sub_f32_e32 v88, v29, v111
	v_min_f32_e32 v88, 0, v88
	v_mul_f32_e32 v98, v98, v112
	v_mul_f32_e32 v88, 0x3fb8aa3b, v88
	v_cndmask_b32_e64 v120, v98, 0, s[46:47]
	v_mul_f32_e32 v98, v95, v119
	v_exp_f32_e32 v95, v88
	v_mul_f32_e32 v98, v98, v113
	v_cndmask_b32_e64 v121, 0, v98, s[48:49]
	v_pk_mul_f32 v[88:89], v[96:97], v[116:117]
	v_pk_mul_f32 v[94:95], v[96:97], v[94:95]
	v_pk_mul_f32 v[88:89], v[88:89], v[114:115]
	v_pk_mul_f32 v[92:93], v[94:95], v[92:93]
	global_load_dwordx4 v[94:97], v[86:87], off
	global_load_dwordx4 v[98:101], v[86:87], off offset:64
	global_load_dwordx4 v[104:107], v[86:87], off offset:128
	global_load_dwordx4 v[108:111], v[86:87], off offset:192
	s_waitcnt vmcnt(3)
	v_mfma_f32_16x16x32_bf16 v[94:97], v[94:97], v[20:23], 0
	ds_read_b128 v[112:115], v186 offset:192
	ds_read_b128 v[116:119], v187 offset:192
	v_cvt_pk_bf16_f32 v90, v90, v91
	v_cvt_pk_bf16_f32 v91, v92, v93
	s_waitcnt vmcnt(2)
	v_mfma_f32_16x16x32_bf16 v[94:97], v[98:101], v[16:19], v[94:97]
	s_waitcnt lgkmcnt(1)
	v_sub_f32_e32 v86, v29, v112
	v_min_f32_e32 v86, 0, v86
	v_mul_f32_e32 v86, 0x3fb8aa3b, v86
	s_waitcnt vmcnt(1)
	v_mfma_f32_16x16x32_bf16 v[94:97], v[104:107], v[8:11], v[94:97]
	v_exp_f32_e32 v86, v86
	v_sub_f32_e32 v87, v29, v115
	v_min_f32_e32 v87, 0, v87
	s_waitcnt vmcnt(0)
	v_mfma_f32_16x16x32_bf16 v[94:97], v[108:111], v[12:15], v[94:97]
	s_waitcnt lgkmcnt(0)
	v_mul_f32_e32 v86, v116, v86
	v_mul_f32_e32 v87, 0x3fb8aa3b, v87
	v_exp_f32_e32 v87, v87
	s_nop 3
	v_mul_f32_e32 v86, v86, v94
	v_cndmask_b32_e64 v98, v86, 0, s[46:47]
	v_sub_f32_e32 v86, v29, v113
	v_min_f32_e32 v86, 0, v86
	v_mul_f32_e32 v86, 0x3fb8aa3b, v86
	v_exp_f32_e32 v86, v86
	s_nop 0
	v_mul_f32_e32 v86, v117, v86
	v_mul_f32_e32 v86, v86, v95
	v_cndmask_b32_e64 v99, 0, v86, s[48:49]
	v_sub_f32_e32 v86, v29, v114
	v_min_f32_e32 v86, 0, v86
	v_mul_f32_e32 v86, 0x3fb8aa3b, v86
	v_exp_f32_e32 v86, v86
	v_cvt_pk_bf16_f32 v92, v98, v99
	v_mul_f32_e32 v98, 0x3fb8aa3b, v102
	v_mul_f32_e32 v102, 0x3fb8aa3b, v103
	v_pk_mul_f32 v[86:87], v[118:119], v[86:87]
	v_exp_f32_e32 v178, v98
	v_pk_mul_f32 v[94:95], v[86:87], v[96:97]
	v_cvt_pk_bf16_f32 v87, v88, v89
	v_cvt_pk_bf16_f32 v93, v94, v95
	v_cndmask_b32_e64 v88, v87, 0, s[52:53]
	v_lshrrev_b32_e32 v87, 16, v87
	v_cndmask_b32_e64 v94, v93, 0, s[52:53]
	v_lshrrev_b32_e32 v93, 16, v93
	v_cndmask_b32_e64 v87, v87, 0, s[50:51]
	v_cndmask_b32_e64 v93, v93, 0, s[50:51]
	v_perm_b32 v87, v87, v88, s0
	v_perm_b32 v93, v93, v94, s0
	s_lshl_b64 s[0:1], s[18:19], 12
	s_lshl_b64 s[18:19], s[20:21], 6
	s_add_u32 s0, s18, s0
	s_addc_u32 s1, s19, s1
	v_mov_b32_e32 v95, s1
	v_or_b32_e32 v94, s0, v166
	v_lshlrev_b64 v[94:95], 8, v[94:95]
	v_lshl_add_u64 v[142:143], v[162:163], 0, v[94:95]
	v_cvt_pk_bf16_f32 v86, v120, v121
	global_load_dwordx4 v[106:109], v[142:143], off
	global_load_dwordx4 v[110:113], v[142:143], off offset:64
	global_load_dwordx4 v[114:117], v[142:143], off offset:128
	global_load_dwordx4 v[118:121], v[142:143], off offset:192
	s_waitcnt vmcnt(3)
	v_mfma_f32_16x16x32_bf16 v[94:97], v[106:109], v[4:7], 0
	v_exp_f32_e32 v174, v102
	v_mov_b32_e32 v88, v33
	v_mfma_f32_16x16x32_bf16 v[98:101], v[106:109], v[62:65], 0
	v_mov_b32_e32 v89, v33
	v_mfma_f32_16x16x32_bf16 v[102:105], v[106:109], v[46:49], 0
	v_mfma_f32_16x16x32_bf16 v[106:109], v[106:109], v[20:23], 0
	s_waitcnt vmcnt(2)
	v_mfma_f32_16x16x32_bf16 v[94:97], v[110:113], v[0:3], v[94:97]
	v_mfma_f32_16x16x32_bf16 v[98:101], v[110:113], v[58:61], v[98:101]
	v_mfma_f32_16x16x32_bf16 v[102:105], v[110:113], v[42:45], v[102:105]
	v_mfma_f32_16x16x32_bf16 v[106:109], v[110:113], v[16:19], v[106:109]
	v_add_co_u32_e64 v110, s[0:1], s76, v142
	s_nop 1
	v_addc_co_u32_e64 v111, s[0:1], 0, v143, s[0:1]
	v_add_co_u32_e64 v126, s[0:1], s74, v142
	s_waitcnt vmcnt(1)
	v_mfma_f32_16x16x32_bf16 v[94:97], v[114:117], v[70:73], v[94:97]
	v_addc_co_u32_e64 v127, s[0:1], 0, v143, s[0:1]
	global_load_dwordx4 v[122:125], v[126:127], off offset:-4096
	global_load_dwordx4 v[128:131], v[110:111], off offset:64
	global_load_dwordx4 v[132:135], v[110:111], off offset:128
	global_load_dwordx4 v[136:139], v[110:111], off offset:192
	v_mfma_f32_16x16x32_bf16 v[98:101], v[114:117], v[54:57], v[98:101]
	v_mfma_f32_16x16x32_bf16 v[102:105], v[114:117], v[38:41], v[102:105]
	v_mfma_f32_16x16x32_bf16 v[106:109], v[114:117], v[8:11], v[106:109]
	s_waitcnt vmcnt(4)
	v_mfma_f32_16x16x32_bf16 v[94:97], v[118:121], v[66:69], v[94:97]
	v_mfma_f32_16x16x32_bf16 v[98:101], v[118:121], v[50:53], v[98:101]
	v_mfma_f32_16x16x32_bf16 v[102:105], v[118:121], v[24:27], v[102:105]
	s_nop 5
	v_mul_f32_e64 v96, v178, v96
	v_mul_f32_e64 v97, v178, v97
	v_pk_mul_f32 v[94:95], v[178:179], v[94:95] op_sel_hi:[0,1]
	v_mfma_f32_16x16x32_bf16 v[106:109], v[118:121], v[12:15], v[106:109]
	s_waitcnt vmcnt(3)
	v_mfma_f32_16x16x32_bf16 v[110:113], v[122:125], v[4:7], 0
	v_mul_f32_e64 v104, v176, v104
	v_mul_f32_e64 v105, v176, v105
	v_pk_mul_f32 v[102:103], v[176:177], v[102:103] op_sel_hi:[0,1]
	s_nop 2
	v_pk_mul_f32 v[108:109], v[28:29], v[108:109] op_sel_hi:[0,1]
	v_mfma_f32_16x16x32_bf16 v[114:117], v[122:125], v[62:65], 0
	v_mul_f32_e64 v106, v28, v106
	v_mul_f32_e64 v107, v28, v107
	v_mfma_f32_16x16x32_bf16 v[118:121], v[122:125], v[46:49], 0
	v_mfma_f32_16x16x32_bf16 v[122:125], v[122:125], v[20:23], 0
	s_waitcnt vmcnt(2)
	v_mfma_f32_16x16x32_bf16 v[110:113], v[128:131], v[0:3], v[110:113]
	v_mfma_f32_16x16x32_bf16 v[114:117], v[128:131], v[58:61], v[114:117]
	v_mfma_f32_16x16x32_bf16 v[118:121], v[128:131], v[42:45], v[118:121]
	v_mfma_f32_16x16x32_bf16 v[122:125], v[128:131], v[16:19], v[122:125]
	s_waitcnt vmcnt(1)
	v_mfma_f32_16x16x32_bf16 v[110:113], v[132:135], v[70:73], v[110:113]
	v_mfma_f32_16x16x32_bf16 v[114:117], v[132:135], v[54:57], v[114:117]
	v_mfma_f32_16x16x32_bf16 v[118:121], v[132:135], v[38:41], v[118:121]
	v_mfma_f32_16x16x32_bf16 v[122:125], v[132:135], v[8:11], v[122:125]
	s_waitcnt vmcnt(0)
	v_mfma_f32_16x16x32_bf16 v[110:113], v[136:139], v[66:69], v[110:113]
	v_mfma_f32_16x16x32_bf16 v[114:117], v[136:139], v[50:53], v[114:117]
	v_mfma_f32_16x16x32_bf16 v[118:121], v[136:139], v[24:27], v[118:121]
	s_nop 5
	v_mul_f32_e64 v112, v178, v112
	v_mul_f32_e64 v113, v178, v113
	v_pk_mul_f32 v[110:111], v[178:179], v[110:111] op_sel_hi:[0,1]
	v_pk_mul_f32 v[116:117], v[174:175], v[116:117] op_sel_hi:[0,1]
	v_mfma_f32_16x16x32_bf16 v[122:125], v[136:139], v[12:15], v[122:125]
	global_load_dwordx4 v[138:141], v[126:127], off
	global_load_dwordx4 v[144:147], v[126:127], off offset:64
	global_load_dwordx4 v[148:151], v[126:127], off offset:128
	global_load_dwordx4 v[152:155], v[126:127], off offset:192
	v_pk_mul_f32 v[114:115], v[174:175], v[114:115] op_sel_hi:[0,1]
	s_waitcnt vmcnt(3)
	v_mfma_f32_16x16x32_bf16 v[126:129], v[138:141], v[4:7], 0
	v_mul_f32_e64 v120, v176, v120
	v_mul_f32_e64 v121, v176, v121
	v_pk_mul_f32 v[118:119], v[176:177], v[118:119] op_sel_hi:[0,1]
	v_pk_mul_f32 v[124:125], v[28:29], v[124:125] op_sel_hi:[0,1]
	v_mfma_f32_16x16x32_bf16 v[130:133], v[138:141], v[62:65], 0
	v_mul_f32_e64 v122, v28, v122
	v_mul_f32_e64 v123, v28, v123
	v_mfma_f32_16x16x32_bf16 v[134:137], v[138:141], v[46:49], 0
	v_mfma_f32_16x16x32_bf16 v[138:141], v[138:141], v[20:23], 0
	s_waitcnt vmcnt(2)
	v_mfma_f32_16x16x32_bf16 v[126:129], v[144:147], v[0:3], v[126:129]
	v_mfma_f32_16x16x32_bf16 v[130:133], v[144:147], v[58:61], v[130:133]
	v_mfma_f32_16x16x32_bf16 v[134:137], v[144:147], v[42:45], v[134:137]
	v_mfma_f32_16x16x32_bf16 v[138:141], v[144:147], v[16:19], v[138:141]
	s_waitcnt vmcnt(1)
	v_mfma_f32_16x16x32_bf16 v[126:129], v[148:151], v[70:73], v[126:129]
	v_mfma_f32_16x16x32_bf16 v[130:133], v[148:151], v[54:57], v[130:133]
	v_mfma_f32_16x16x32_bf16 v[134:137], v[148:151], v[38:41], v[134:137]
	v_mfma_f32_16x16x32_bf16 v[138:141], v[148:151], v[8:11], v[138:141]
	s_waitcnt vmcnt(0)
	v_mfma_f32_16x16x32_bf16 v[126:129], v[152:155], v[66:69], v[126:129]
	v_mfma_f32_16x16x32_bf16 v[130:133], v[152:155], v[50:53], v[130:133]
	v_mfma_f32_16x16x32_bf16 v[134:137], v[152:155], v[24:27], v[134:137]
	s_nop 5
	v_mul_f32_e64 v128, v178, v128
	v_mul_f32_e64 v129, v178, v129
	v_pk_mul_f32 v[126:127], v[178:179], v[126:127] op_sel_hi:[0,1]
	v_pk_mul_f32 v[132:133], v[174:175], v[132:133] op_sel_hi:[0,1]
	v_mfma_f32_16x16x32_bf16 v[138:141], v[152:155], v[12:15], v[138:141]
	v_add_co_u32_e64 v154, s[0:1], s77, v142
	v_pk_mul_f32 v[130:131], v[174:175], v[130:131] op_sel_hi:[0,1]
	s_nop 0
	v_addc_co_u32_e64 v155, s[0:1], 0, v143, s[0:1]
	global_load_dwordx4 v[142:145], v[154:155], off
	global_load_dwordx4 v[146:149], v[154:155], off offset:64
	global_load_dwordx4 v[150:153], v[154:155], off offset:128
	s_nop 0
	global_load_dwordx4 v[154:157], v[154:155], off offset:192
	s_waitcnt vmcnt(3)
	v_mfma_f32_16x16x32_bf16 v[4:7], v[142:145], v[4:7], 0
	v_mul_f32_e64 v136, v176, v136
	v_mul_f32_e64 v137, v176, v137
	v_pk_mul_f32 v[134:135], v[176:177], v[134:135] op_sel_hi:[0,1]
	s_waitcnt vmcnt(2)
	v_mfma_f32_16x16x32_bf16 v[0:3], v[146:149], v[0:3], v[4:7]
	v_mul_f32_e64 v140, v28, v140
	v_mul_f32_e64 v141, v28, v141
	v_pk_mul_f32 v[138:139], v[28:29], v[138:139] op_sel_hi:[0,1]
	s_add_u32 s0, s62, s16
	s_waitcnt vmcnt(1)
	v_mfma_f32_16x16x32_bf16 v[0:3], v[150:153], v[70:73], v[0:3]
	s_addc_u32 s1, s63, s17
	s_waitcnt vmcnt(0)
	v_mfma_f32_16x16x32_bf16 v[0:3], v[154:157], v[66:69], v[0:3]
	s_nop 7
	v_pk_mul_f32 v[68:69], v[178:179], v[2:3] op_sel_hi:[0,1]
	v_pk_mul_f32 v[66:67], v[178:179], v[0:1] op_sel_hi:[0,1]
	v_mfma_f32_16x16x32_bf16 v[0:3], v[142:145], v[62:65], 0
	v_mfma_f32_16x16x32_bf16 v[0:3], v[146:149], v[58:61], v[0:3]
	v_mfma_f32_16x16x32_bf16 v[0:3], v[150:153], v[54:57], v[0:3]
	v_mfma_f32_16x16x32_bf16 v[0:3], v[154:157], v[50:53], v[0:3]
	s_nop 7
	v_pk_mul_f32 v[72:73], v[174:175], v[2:3] op_sel_hi:[0,1]
	v_pk_mul_f32 v[70:71], v[174:175], v[0:1] op_sel_hi:[0,1]
	v_mfma_f32_16x16x32_bf16 v[0:3], v[142:145], v[46:49], 0
	v_mfma_f32_16x16x32_bf16 v[0:3], v[146:149], v[42:45], v[0:3]
	v_mfma_f32_16x16x32_bf16 v[0:3], v[150:153], v[38:41], v[0:3]
	v_mfma_f32_16x16x32_bf16 v[0:3], v[154:157], v[24:27], v[0:3]
	s_nop 7
	v_pk_mul_f32 v[26:27], v[176:177], v[2:3] op_sel_hi:[0,1]
	v_pk_mul_f32 v[24:25], v[176:177], v[0:1] op_sel_hi:[0,1]
	v_mfma_f32_16x16x32_bf16 v[0:3], v[142:145], v[20:23], 0
	v_mfma_f32_16x16x32_bf16 v[0:3], v[146:149], v[16:19], v[0:3]
	v_mul_f32_e64 v18, v174, v100
	v_mul_f32_e64 v19, v174, v101
	v_pk_mul_f32 v[16:17], v[174:175], v[98:99] op_sel_hi:[0,1]
	v_mfma_f32_16x16x32_bf16 v[0:3], v[150:153], v[8:11], v[0:3]
	v_mfma_f32_16x16x32_bf16 v[0:3], v[154:157], v[12:15], v[0:3]
	s_nop 7
	v_pk_mul_f32 v[10:11], v[28:29], v[2:3] op_sel_hi:[0,1]
	v_pk_mul_f32 v[8:9], v[28:29], v[0:1] op_sel_hi:[0,1]
	ds_read_b64_tr_b16 v[2:3], v213 offset:2560
	ds_read_b64_tr_b16 v[0:1], v213
	ds_read_b64_tr_b16 v[4:5], v213 offset:32
	ds_read_b64_tr_b16 v[12:13], v213 offset:5120
	ds_read_b64_tr_b16 v[14:15], v213 offset:7680
	s_waitcnt lgkmcnt(3)
	v_mfma_f32_16x16x32_bf16 v[94:97], v[0:3], v[30:33], v[94:97]
	v_mfma_f32_16x16x32_bf16 v[50:53], v[0:3], v[74:77], v[16:19]
	v_mfma_f32_16x16x32_bf16 v[16:19], v[0:3], v[78:81], v[102:105]
	v_mfma_f32_16x16x32_bf16 v[0:3], v[0:3], v[82:85], v[106:109]
	s_waitcnt lgkmcnt(0)
	v_mfma_f32_16x16x32_bf16 v[38:41], v[12:15], v[86:89], v[16:19]
	v_mfma_f32_16x16x32_bf16 v[12:15], v[12:15], v[90:93], v[0:3]
	ds_read_b64_tr_b16 v[6:7], v213 offset:2592
	s_nop 3
	ds_read_b64_tr_b16 v[0:1], v213 offset:5152
	ds_read_b64_tr_b16 v[2:3], v213 offset:7712
	s_waitcnt lgkmcnt(2)
	v_mfma_f32_16x16x32_bf16 v[62:65], v[4:7], v[30:33], v[110:113]
	v_mfma_f32_16x16x32_bf16 v[46:49], v[4:7], v[74:77], v[114:117]
	v_mfma_f32_16x16x32_bf16 v[16:19], v[4:7], v[78:81], v[118:121]
	v_mfma_f32_16x16x32_bf16 v[4:7], v[4:7], v[82:85], v[122:125]
	s_waitcnt lgkmcnt(0)
	v_mfma_f32_16x16x32_bf16 v[20:23], v[0:3], v[86:89], v[16:19]
	v_mfma_f32_16x16x32_bf16 v[4:7], v[0:3], v[90:93], v[4:7]
	ds_read_b64_tr_b16 v[0:1], v213 offset:64
	ds_read_b64_tr_b16 v[2:3], v213 offset:2624
	ds_read_b64_tr_b16 v[54:55], v213 offset:5184
	ds_read_b64_tr_b16 v[56:57], v213 offset:7744
	ds_read_b64_tr_b16 v[98:99], v213 offset:96
	ds_read_b64_tr_b16 v[100:101], v213 offset:2656
	ds_read_b64_tr_b16 v[102:103], v213 offset:5216
	ds_read_b64_tr_b16 v[104:105], v213 offset:7776
	s_waitcnt lgkmcnt(6)
	v_mfma_f32_16x16x32_bf16 v[58:61], v[0:3], v[30:33], v[126:129]
	v_mfma_f32_16x16x32_bf16 v[42:45], v[0:3], v[74:77], v[130:133]
	v_mfma_f32_16x16x32_bf16 v[16:19], v[0:3], v[78:81], v[134:137]
	v_mfma_f32_16x16x32_bf16 v[0:3], v[0:3], v[82:85], v[138:141]
	s_waitcnt lgkmcnt(4)
	v_mfma_f32_16x16x32_bf16 v[16:19], v[54:57], v[86:89], v[16:19]
	v_mfma_f32_16x16x32_bf16 v[0:3], v[54:57], v[90:93], v[0:3]
	s_waitcnt lgkmcnt(2)
	v_mfma_f32_16x16x32_bf16 v[54:57], v[98:101], v[30:33], v[66:69]
	v_add_u32_e32 v32, v192, v158
	v_mfma_f32_16x16x32_bf16 v[28:31], v[98:101], v[74:77], v[70:73]
	s_nop 0
	ds_read_b64 v[68:69], v32
	v_lshlrev_b32_e32 v32, 1, v170
	global_load_dword v70, v33, s[0:1] offset:768
	s_add_u32 s0, s2, s14
	s_addc_u32 s1, s3, s15
	v_mfma_f32_16x16x32_bf16 v[24:27], v[98:101], v[78:81], v[24:27]
	v_mov_b64_e32 v[78:79], s[0:1]
	v_mad_i64_i32 v[66:67], s[0:1], v172, s96, v[78:79]
	v_lshl_add_u64 v[72:73], v[66:67], 0, v[32:33]
	global_load_dwordx2 v[74:75], v[72:73], off
	global_load_dwordx2 v[202:203], v[72:73], off offset:32
	global_load_dwordx2 v[216:217], v[72:73], off offset:64
	global_load_dwordx2 v[248:249], v[72:73], off offset:96
	s_waitcnt lgkmcnt(0)
	v_lshlrev_b32_e32 v66, 16, v68
	v_and_b32_e32 v67, 0xffff0000, v68
	v_mfma_f32_16x16x32_bf16 v[8:11], v[98:101], v[82:85], v[8:11]
	s_waitcnt vmcnt(4)
	v_pk_fma_f32 v[66:67], v[70:71], v[66:67], v[94:95] op_sel_hi:[0,1,1]
	v_mfma_f32_16x16x32_bf16 v[24:27], v[102:105], v[86:89], v[24:27]
	s_waitcnt vmcnt(3)
	v_lshlrev_b32_e32 v76, 16, v74
	v_mul_f32_e32 v68, 0xbfb8aa3b, v76
	v_exp_f32_e32 v68, v68
	v_and_b32_e32 v77, 0xffff0000, v74
	v_lshlrev_b32_e32 v74, 16, v75
	v_mul_f32_e32 v71, 0xbfb8aa3b, v74
	v_add_f32_e32 v68, 1.0, v68
	v_rcp_f32_e32 v80, v68
	v_mul_f32_e32 v68, 0xbfb8aa3b, v77
	v_exp_f32_e32 v68, v68
	v_exp_f32_e32 v71, v71
	v_pk_mul_f32 v[66:67], v[66:67], v[76:77]
	v_and_b32_e32 v75, 0xffff0000, v75
	v_add_f32_e32 v68, 1.0, v68
	v_rcp_f32_e32 v81, v68
	v_add_f32_e32 v71, 1.0, v71
	v_mfma_f32_16x16x32_bf16 v[8:11], v[102:105], v[90:93], v[8:11]
	v_mul_f32_e64 v66, v66, v80
	v_mul_f32_e64 v67, v67, v81
	v_mul_f32_e32 v68, v67, v67
	v_pk_fma_f32 v[76:77], v[66:67], v[66:67], v[68:69] op_sel_hi:[1,1,0]
	v_lshlrev_b32_e32 v68, 16, v69
	v_and_b32_e32 v69, 0xffff0000, v69
	v_rcp_f32_e32 v80, v71
	v_pk_fma_f32 v[68:69], v[70:71], v[68:69], v[96:97] op_sel_hi:[0,1,1]
	v_mul_f32_e32 v71, 0xbfb8aa3b, v75
	v_exp_f32_e32 v71, v71
	v_pk_mul_f32 v[68:69], v[68:69], v[74:75]
	v_add_f32_e32 v71, 1.0, v71
	v_rcp_f32_e32 v81, v71
	v_add_u32_e32 v71, v192, v193
	v_pk_mul_f32 v[68:69], v[68:69], v[80:81]
	v_pk_fma_f32 v[74:75], v[68:69], v[68:69], v[76:77]
	v_mul_f32_e32 v76, v69, v69
	v_pk_add_f32 v[74:75], v[76:77], v[74:75] op_sel_hi:[0,1]
	ds_read_b64 v[76:77], v71
	s_waitcnt lgkmcnt(0)
	v_lshlrev_b32_e32 v82, 16, v76
	v_and_b32_e32 v83, 0xffff0000, v76
	s_waitcnt vmcnt(2)
	v_mov_b64_e32 v[80:81], v[202:203]
	v_lshlrev_b32_e32 v84, 16, v80
	v_mul_f32_e32 v71, 0xbfb8aa3b, v84
	v_exp_f32_e32 v71, v71
	v_and_b32_e32 v85, 0xffff0000, v80
	v_lshlrev_b32_e32 v80, 16, v81
	v_and_b32_e32 v81, 0xffff0000, v81
	v_add_f32_e32 v71, 1.0, v71
	v_rcp_f32_e32 v86, v71
	v_pk_fma_f32 v[62:63], v[70:71], v[82:83], v[62:63] op_sel_hi:[0,1,1]
	v_mul_f32_e32 v71, 0xbfb8aa3b, v85
	v_exp_f32_e32 v71, v71
	v_pk_mul_f32 v[62:63], v[62:63], v[84:85]
	v_add_f32_e32 v71, 1.0, v71
	v_rcp_f32_e32 v87, v71
	v_mul_f32_e32 v71, 0xbfb8aa3b, v80
	v_exp_f32_e32 v71, v71
	v_pk_mul_f32 v[62:63], v[62:63], v[86:87]
	s_nop 0
	v_pk_fma_f32 v[74:75], v[62:63], v[62:63], v[74:75]
	v_mul_f32_e32 v76, v63, v63
	v_pk_add_f32 v[74:75], v[76:77], v[74:75] op_sel_hi:[0,1]
	v_lshlrev_b32_e32 v76, 16, v77
	v_and_b32_e32 v77, 0xffff0000, v77
	v_add_f32_e32 v71, 1.0, v71
	v_pk_fma_f32 v[64:65], v[70:71], v[76:77], v[64:65] op_sel_hi:[0,1,1]
	v_rcp_f32_e32 v82, v71
	v_pk_mul_f32 v[64:65], v[64:65], v[80:81]
	v_mul_f32_e32 v71, 0xbfb8aa3b, v81
	v_exp_f32_e32 v71, v71
	s_waitcnt vmcnt(1)
	v_mov_b64_e32 v[80:81], v[216:217]
	v_lshlrev_b32_e32 v84, 16, v80
	v_add_f32_e32 v71, 1.0, v71
	v_rcp_f32_e32 v83, v71
	v_add_u32_e32 v71, v192, v194
	v_and_b32_e32 v85, 0xffff0000, v80
	v_lshlrev_b32_e32 v80, 16, v81
	v_pk_mul_f32 v[64:65], v[64:65], v[82:83]
	v_and_b32_e32 v81, 0xffff0000, v81
	v_pk_fma_f32 v[74:75], v[64:65], v[64:65], v[74:75]
	v_mul_f32_e32 v76, v65, v65
	v_pk_add_f32 v[74:75], v[76:77], v[74:75] op_sel_hi:[0,1]
	ds_read_b64 v[76:77], v71
	v_mul_f32_e32 v71, 0xbfb8aa3b, v84
	v_exp_f32_e32 v71, v71
	s_waitcnt lgkmcnt(0)
	v_lshlrev_b32_e32 v82, 16, v76
	v_and_b32_e32 v83, 0xffff0000, v76
	v_add_f32_e32 v71, 1.0, v71
	v_rcp_f32_e32 v86, v71
	v_pk_fma_f32 v[58:59], v[70:71], v[82:83], v[58:59] op_sel_hi:[0,1,1]
	v_mul_f32_e32 v71, 0xbfb8aa3b, v85
	v_exp_f32_e32 v71, v71
	v_pk_mul_f32 v[58:59], v[58:59], v[84:85]
	v_add_f32_e32 v71, 1.0, v71
	v_rcp_f32_e32 v87, v71
	v_mul_f32_e32 v71, 0xbfb8aa3b, v80
	v_exp_f32_e32 v71, v71
	v_pk_mul_f32 v[58:59], v[58:59], v[86:87]
	s_nop 0
	v_pk_fma_f32 v[74:75], v[58:59], v[58:59], v[74:75]
	v_mul_f32_e32 v76, v59, v59
	v_pk_add_f32 v[74:75], v[76:77], v[74:75] op_sel_hi:[0,1]
	v_lshlrev_b32_e32 v76, 16, v77
	v_and_b32_e32 v77, 0xffff0000, v77
	v_add_f32_e32 v71, 1.0, v71
	v_pk_fma_f32 v[60:61], v[70:71], v[76:77], v[60:61] op_sel_hi:[0,1,1]
	v_rcp_f32_e32 v82, v71
	v_pk_mul_f32 v[60:61], v[60:61], v[80:81]
	v_mul_f32_e32 v71, 0xbfb8aa3b, v81
	v_exp_f32_e32 v71, v71
	s_nop 0
	v_add_f32_e32 v71, 1.0, v71
	v_rcp_f32_e32 v83, v71
	v_add_u32_e32 v71, v192, v195
	v_pk_mul_f32 v[60:61], v[60:61], v[82:83]
	s_nop 0
	v_pk_fma_f32 v[74:75], v[60:61], v[60:61], v[74:75]
	v_mul_f32_e32 v76, v61, v61
	v_pk_add_f32 v[74:75], v[76:77], v[74:75] op_sel_hi:[0,1]
	ds_read_b64 v[76:77], v71
	s_waitcnt lgkmcnt(0)
	v_lshlrev_b32_e32 v72, 16, v76
	v_and_b32_e32 v73, 0xffff0000, v76
	s_waitcnt vmcnt(0)
	v_mov_b64_e32 v[80:81], v[248:249]
	v_lshlrev_b32_e32 v82, 16, v80
	v_mul_f32_e32 v71, 0xbfb8aa3b, v82
	v_exp_f32_e32 v71, v71
	v_and_b32_e32 v83, 0xffff0000, v80
	v_lshlrev_b32_e32 v76, 16, v81
	v_add_f32_e32 v71, 1.0, v71
	v_rcp_f32_e32 v84, v71
	v_pk_fma_f32 v[54:55], v[70:71], v[72:73], v[54:55] op_sel_hi:[0,1,1]
	v_mul_f32_e32 v71, 0xbfb8aa3b, v83
	v_exp_f32_e32 v71, v71
	v_pk_mul_f32 v[54:55], v[54:55], v[82:83]
	v_add_f32_e32 v71, 1.0, v71
	v_rcp_f32_e32 v85, v71
	v_mul_f32_e32 v71, 0xbfb8aa3b, v76
	v_exp_f32_e32 v71, v71
	v_pk_mul_f32 v[72:73], v[54:55], v[84:85]
	s_nop 0
	v_pk_fma_f32 v[54:55], v[72:73], v[72:73], v[74:75]
	v_mul_f32_e32 v74, v73, v73
	v_pk_add_f32 v[54:55], v[74:75], v[54:55] op_sel_hi:[0,1]
	v_lshlrev_b32_e32 v74, 16, v77
	v_and_b32_e32 v75, 0xffff0000, v77
	v_and_b32_e32 v77, 0xffff0000, v81
	v_add_f32_e32 v71, 1.0, v71
	v_rcp_f32_e32 v80, v71
	v_pk_fma_f32 v[56:57], v[70:71], v[74:75], v[56:57] op_sel_hi:[0,1,1]
	v_mul_f32_e32 v71, 0xbfb8aa3b, v77
	v_exp_f32_e32 v71, v71
	v_pk_mul_f32 v[56:57], v[56:57], v[76:77]
	v_or_b32_e32 v76, s28, v208
	v_add_f32_e32 v71, 1.0, v71
	v_rcp_f32_e32 v81, v71
	s_nop 0
	v_pk_mul_f32 v[56:57], v[56:57], v[80:81]
	s_nop 0
	v_pk_fma_f32 v[54:55], v[56:57], v[56:57], v[54:55]
	v_mul_f32_e32 v74, v57, v57
	v_pk_add_f32 v[110:111], v[74:75], v[54:55] op_sel_hi:[0,1]
	v_or_b32_e32 v54, s28, v196
	v_mad_i64_i32 v[74:75], s[0:1], v54, s96, v[78:79]
	v_lshl_add_u64 v[74:75], v[74:75], 0, v[32:33]
	global_load_dwordx2 v[126:127], v[74:75], off
	global_load_dwordx2 v[122:123], v[74:75], off offset:32
	global_load_dwordx2 v[116:117], v[74:75], off offset:64
	global_load_dwordx2 v[112:113], v[74:75], off offset:96
	v_mad_i64_i32 v[74:75], s[0:1], v76, s96, v[78:79]
	v_lshl_add_u64 v[74:75], v[74:75], 0, v[32:33]
	global_load_dwordx2 v[106:107], v[74:75], off
	global_load_dwordx2 v[102:103], v[74:75], off offset:32
	global_load_dwordx2 v[98:99], v[74:75], off offset:64
	global_load_dwordx2 v[94:95], v[74:75], off offset:96
	v_or_b32_e32 v74, s28, v210
	v_mad_i64_i32 v[78:79], s[0:1], v74, s96, v[78:79]
	v_lshl_add_u64 v[78:79], v[78:79], 0, v[32:33]
	global_load_dwordx2 v[90:91], v[78:79], off
	global_load_dwordx2 v[86:87], v[78:79], off offset:32
	global_load_dwordx2 v[82:83], v[78:79], off offset:64
	v_add_u32_e32 v55, v197, v158
	global_load_dwordx2 v[78:79], v[78:79], off offset:96
	v_add_u32_e32 v32, v211, v193
	ds_read_b64 v[120:121], v55
	ds_read_b64 v[88:89], v32
	v_add_u32_e32 v55, v197, v193
	v_add_u32_e32 v32, v211, v194
	ds_read_b64 v[124:125], v55
	ds_read_b64 v[84:85], v32
	v_add_u32_e32 v55, v197, v194
	v_add_u32_e32 v32, v211, v195
	ds_read_b64 v[118:119], v55
	ds_read_b64 v[80:81], v32
	v_add_u32_e32 v55, v197, v195
	ds_read_b64 v[114:115], v55
	v_add_u32_e32 v55, v209, v158
	ds_read_b64 v[108:109], v55
	v_add_u32_e32 v55, v209, v193
	ds_read_b64 v[104:105], v55
	v_add_u32_e32 v55, v209, v194
	ds_read_b64 v[100:101], v55
	v_add_u32_e32 v55, v209, v195
	ds_read_b64 v[96:97], v55
	v_add_u32_e32 v55, v211, v158
	ds_read_b64 v[92:93], v55
	s_lshl_b32 s0, s26, 11
	v_mov_b32_e32 v55, v110
	s_add_i32 s14, s0, 0
	s_nop 0
	v_permlane16_swap_b32_e32 v110, v55
	s_add_i32 s14, s14, 0x15000
	v_add_f32_e32 v55, v110, v55
	s_add_i32 s0, s14, s23
	v_mov_b32_e32 v71, v55
	v_lshl_add_u32 v32, v166, 2, s0
	s_nop 0
	v_permlane32_swap_b32_e32 v55, v71
	s_and_saveexec_b64 s[0:1], s[42:43]
	v_add_f32_e32 v55, v55, v71
	ds_write_b32 v32, v55
	s_or_b64 exec, exec, s[0:1]
	s_waitcnt vmcnt(11)
	v_lshlrev_b32_e32 v128, 16, v126
	v_mul_f32_e32 v55, 0xbfb8aa3b, v128
	v_exp_f32_e32 v55, v55
	v_and_b32_e32 v129, 0xffff0000, v126
	v_lshlrev_b32_e32 v126, 16, v127
	v_mov_b32_e32 v71, v70
	v_add_f32_e32 v55, 1.0, v55
	v_rcp_f32_e32 v130, v55
	v_mul_f32_e32 v55, 0xbfb8aa3b, v129
	v_exp_f32_e32 v55, v55
	s_waitcnt lgkmcnt(11)
	v_lshlrev_b32_e32 v110, 16, v120
	v_and_b32_e32 v111, 0xffff0000, v120
	v_pk_fma_f32 v[50:51], v[70:71], v[110:111], v[50:51]
	v_add_f32_e32 v55, 1.0, v55
	v_rcp_f32_e32 v131, v55
	v_mul_f32_e32 v55, 0xbfb8aa3b, v126
	v_exp_f32_e32 v55, v55
	v_and_b32_e32 v127, 0xffff0000, v127
	v_pk_mul_f32 v[50:51], v[50:51], v[128:129]
	v_lshlrev_b32_e32 v120, 16, v121
	v_add_f32_e32 v55, 1.0, v55
	v_rcp_f32_e32 v128, v55
	v_mul_f32_e32 v55, 0xbfb8aa3b, v127
	v_exp_f32_e32 v55, v55
	v_and_b32_e32 v121, 0xffff0000, v121
	v_pk_fma_f32 v[52:53], v[70:71], v[120:121], v[52:53]
	v_pk_mul_f32 v[50:51], v[50:51], v[130:131]
	v_pk_mul_f32 v[52:53], v[52:53], v[126:127]
	v_add_f32_e32 v55, 1.0, v55
	s_waitcnt vmcnt(10)
	v_lshlrev_b32_e32 v126, 16, v122
	v_rcp_f32_e32 v129, v55
	v_mul_f32_e32 v55, 0xbfb8aa3b, v126
	v_exp_f32_e32 v55, v55
	v_and_b32_e32 v127, 0xffff0000, v122
	v_pk_mul_f32 v[52:53], v[52:53], v[128:129]
	v_lshlrev_b32_e32 v122, 16, v123
	v_add_f32_e32 v55, 1.0, v55
	v_rcp_f32_e32 v128, v55
	v_mul_f32_e32 v55, 0xbfb8aa3b, v127
	v_exp_f32_e32 v55, v55
	v_mul_f32_e32 v110, v51, v51
	v_pk_fma_f32 v[110:111], v[50:51], v[50:51], v[110:111] op_sel_hi:[1,1,0]
	v_mul_f32_e32 v120, v53, v53
	v_add_f32_e32 v55, 1.0, v55
	v_rcp_f32_e32 v129, v55
	v_mul_f32_e32 v55, 0xbfb8aa3b, v122
	v_exp_f32_e32 v55, v55
	v_pk_fma_f32 v[110:111], v[52:53], v[52:53], v[110:111]
	v_and_b32_e32 v123, 0xffff0000, v123
	v_pk_add_f32 v[110:111], v[120:121], v[110:111] op_sel_hi:[0,1]
	s_waitcnt lgkmcnt(9)
	v_lshlrev_b32_e32 v120, 16, v124
	v_and_b32_e32 v121, 0xffff0000, v124
	v_pk_fma_f32 v[46:47], v[70:71], v[120:121], v[46:47]
	v_add_f32_e32 v55, 1.0, v55
	v_pk_mul_f32 v[46:47], v[46:47], v[126:127]
	v_rcp_f32_e32 v124, v55
	v_mul_f32_e32 v55, 0xbfb8aa3b, v123
	v_pk_mul_f32 v[46:47], v[46:47], v[128:129]
	v_exp_f32_e32 v55, v55
	v_pk_fma_f32 v[110:111], v[46:47], v[46:47], v[110:111]
	v_mul_f32_e32 v120, v47, v47
	v_pk_add_f32 v[110:111], v[120:121], v[110:111] op_sel_hi:[0,1]
	v_lshlrev_b32_e32 v120, 16, v125
	v_and_b32_e32 v121, 0xffff0000, v125
	v_pk_fma_f32 v[48:49], v[70:71], v[120:121], v[48:49]
	v_add_f32_e32 v55, 1.0, v55
	v_pk_mul_f32 v[48:49], v[48:49], v[122:123]
	s_waitcnt vmcnt(9)
	v_lshlrev_b32_e32 v122, 16, v116
	v_rcp_f32_e32 v125, v55
	v_mul_f32_e32 v55, 0xbfb8aa3b, v122
	v_exp_f32_e32 v55, v55
	v_and_b32_e32 v123, 0xffff0000, v116
	v_pk_mul_f32 v[48:49], v[48:49], v[124:125]
	v_add_f32_e32 v55, 1.0, v55
	v_rcp_f32_e32 v124, v55
	v_mul_f32_e32 v55, 0xbfb8aa3b, v123
	v_exp_f32_e32 v55, v55
	v_pk_fma_f32 v[110:111], v[48:49], v[48:49], v[110:111]
	v_mul_f32_e32 v120, v49, v49
	v_pk_add_f32 v[110:111], v[120:121], v[110:111] op_sel_hi:[0,1]
	v_add_f32_e32 v55, 1.0, v55
	v_rcp_f32_e32 v125, v55
	s_waitcnt lgkmcnt(7)
	v_lshlrev_b32_e32 v120, 16, v118
	v_and_b32_e32 v121, 0xffff0000, v118
	v_pk_fma_f32 v[42:43], v[70:71], v[120:121], v[42:43]
	v_lshlrev_b32_e32 v118, 16, v119
	v_pk_mul_f32 v[42:43], v[42:43], v[122:123]
	v_and_b32_e32 v119, 0xffff0000, v119
	v_pk_mul_f32 v[42:43], v[42:43], v[124:125]
	v_pk_fma_f32 v[44:45], v[70:71], v[118:119], v[44:45]
	v_pk_fma_f32 v[110:111], v[42:43], v[42:43], v[110:111]
	v_mul_f32_e32 v116, v43, v43
	v_pk_add_f32 v[110:111], v[116:117], v[110:111] op_sel_hi:[0,1]
	v_lshlrev_b32_e32 v116, 16, v117
	v_mul_f32_e32 v55, 0xbfb8aa3b, v116
	v_exp_f32_e32 v55, v55
	v_and_b32_e32 v117, 0xffff0000, v117
	s_waitcnt vmcnt(8)
	v_lshlrev_b32_e32 v118, 16, v112
	v_pk_mul_f32 v[44:45], v[44:45], v[116:117]
	v_add_f32_e32 v55, 1.0, v55
	v_rcp_f32_e32 v120, v55
	v_mul_f32_e32 v55, 0xbfb8aa3b, v117
	v_exp_f32_e32 v55, v55
	v_and_b32_e32 v119, 0xffff0000, v112
	v_add_f32_e32 v55, 1.0, v55
	v_rcp_f32_e32 v121, v55
	v_mul_f32_e32 v55, 0xbfb8aa3b, v118
	v_exp_f32_e32 v55, v55
	v_pk_mul_f32 v[44:45], v[44:45], v[120:121]
	s_nop 0
	v_pk_fma_f32 v[110:111], v[44:45], v[44:45], v[110:111]
	v_add_f32_e32 v55, 1.0, v55
	v_rcp_f32_e32 v120, v55
	v_mul_f32_e32 v55, 0xbfb8aa3b, v119
	v_exp_f32_e32 v55, v55
	v_mul_f32_e32 v116, v45, v45
	v_pk_add_f32 v[110:111], v[116:117], v[110:111] op_sel_hi:[0,1]
	s_waitcnt lgkmcnt(5)
	v_lshlrev_b32_e32 v116, 16, v114
	v_add_f32_e32 v55, 1.0, v55
	v_rcp_f32_e32 v121, v55
	v_and_b32_e32 v117, 0xffff0000, v114
	v_pk_fma_f32 v[28:29], v[70:71], v[116:117], v[28:29]
	v_lshlrev_b32_e32 v114, 16, v115
	v_pk_mul_f32 v[28:29], v[28:29], v[118:119]
	v_and_b32_e32 v115, 0xffff0000, v115
	v_pk_mul_f32 v[28:29], v[28:29], v[120:121]
	v_pk_fma_f32 v[30:31], v[70:71], v[114:115], v[30:31]
	v_pk_fma_f32 v[110:111], v[28:29], v[28:29], v[110:111]
	v_mul_f32_e32 v112, v29, v29
	v_pk_add_f32 v[110:111], v[112:113], v[110:111] op_sel_hi:[0,1]
	v_lshlrev_b32_e32 v112, 16, v113
	v_mul_f32_e32 v55, 0xbfb8aa3b, v112
	v_exp_f32_e32 v55, v55
	v_and_b32_e32 v113, 0xffff0000, v113
	v_pk_mul_f32 v[30:31], v[30:31], v[112:113]
	v_add_f32_e32 v55, 1.0, v55
	v_rcp_f32_e32 v116, v55
	v_mul_f32_e32 v55, 0xbfb8aa3b, v113
	v_exp_f32_e32 v55, v55
	s_nop 0
	v_add_f32_e32 v55, 1.0, v55
	v_rcp_f32_e32 v117, v55
	s_nop 0
	v_pk_mul_f32 v[30:31], v[30:31], v[116:117]
	s_nop 0
	v_pk_fma_f32 v[110:111], v[30:31], v[30:31], v[110:111]
	v_mul_f32_e32 v112, v31, v31
	v_pk_add_f32 v[110:111], v[112:113], v[110:111] op_sel_hi:[0,1]
	v_mov_b32_e32 v55, v110
	s_nop 1
	v_permlane16_swap_b32_e32 v110, v55
	v_add_f32_e32 v55, v110, v55
	v_mov_b32_e32 v75, v55
	s_nop 1
	v_permlane32_swap_b32_e32 v55, v75
	s_and_saveexec_b64 s[0:1], s[42:43]
	v_add_f32_e32 v55, v55, v75
	ds_write_b32 v32, v55 offset:64
	s_or_b64 exec, exec, s[0:1]
	s_waitcnt vmcnt(7)
	v_lshlrev_b32_e32 v112, 16, v106
	v_mul_f32_e32 v55, 0xbfb8aa3b, v112
	v_exp_f32_e32 v55, v55
	v_and_b32_e32 v113, 0xffff0000, v106
	s_waitcnt lgkmcnt(4)
	v_lshlrev_b32_e32 v110, 16, v108
	v_and_b32_e32 v111, 0xffff0000, v108
	v_add_f32_e32 v55, 1.0, v55
	v_rcp_f32_e32 v114, v55
	v_mul_f32_e32 v55, 0xbfb8aa3b, v113
	v_exp_f32_e32 v55, v55
	v_pk_fma_f32 v[38:39], v[70:71], v[110:111], v[38:39]
	v_lshlrev_b32_e32 v108, 16, v109
	v_pk_mul_f32 v[38:39], v[38:39], v[112:113]
	v_add_f32_e32 v55, 1.0, v55
	v_rcp_f32_e32 v115, v55
	v_and_b32_e32 v109, 0xffff0000, v109
	v_pk_fma_f32 v[40:41], v[70:71], v[108:109], v[40:41]
	v_pk_mul_f32 v[38:39], v[38:39], v[114:115]
	s_nop 0
	v_mul_f32_e32 v106, v39, v39
	v_pk_fma_f32 v[110:111], v[38:39], v[38:39], v[106:107] op_sel_hi:[1,1,0]
	v_lshlrev_b32_e32 v106, 16, v107
	v_mul_f32_e32 v55, 0xbfb8aa3b, v106
	v_exp_f32_e32 v55, v55
	v_and_b32_e32 v107, 0xffff0000, v107
	v_pk_mul_f32 v[40:41], v[40:41], v[106:107]
	v_add_f32_e32 v55, 1.0, v55
	v_rcp_f32_e32 v112, v55
	v_mul_f32_e32 v55, 0xbfb8aa3b, v107
	v_exp_f32_e32 v55, v55
	s_nop 0
	v_add_f32_e32 v55, 1.0, v55
	v_rcp_f32_e32 v113, v55
	s_nop 0
	v_pk_mul_f32 v[40:41], v[40:41], v[112:113]
	s_nop 0
	v_pk_fma_f32 v[106:107], v[40:41], v[40:41], v[110:111]
	s_waitcnt vmcnt(6)
	v_lshlrev_b32_e32 v110, 16, v102
	v_mul_f32_e32 v55, 0xbfb8aa3b, v110
	v_exp_f32_e32 v55, v55
	v_and_b32_e32 v111, 0xffff0000, v102
	v_mul_f32_e32 v108, v41, v41
	v_pk_add_f32 v[106:107], v[108:109], v[106:107] op_sel_hi:[0,1]
	v_add_f32_e32 v55, 1.0, v55
	v_rcp_f32_e32 v112, v55
	v_mul_f32_e32 v55, 0xbfb8aa3b, v111
	v_exp_f32_e32 v55, v55
	s_waitcnt lgkmcnt(3)
	v_lshlrev_b32_e32 v108, 16, v104
	v_and_b32_e32 v109, 0xffff0000, v104
	v_pk_fma_f32 v[20:21], v[70:71], v[108:109], v[20:21]
	v_add_f32_e32 v55, 1.0, v55
	v_rcp_f32_e32 v113, v55
	v_pk_mul_f32 v[20:21], v[20:21], v[110:111]
	v_lshlrev_b32_e32 v104, 16, v105
	v_and_b32_e32 v105, 0xffff0000, v105
	v_pk_mul_f32 v[20:21], v[20:21], v[112:113]
	v_pk_fma_f32 v[22:23], v[70:71], v[104:105], v[22:23]
	v_pk_fma_f32 v[106:107], v[20:21], v[20:21], v[106:107]
	v_mul_f32_e32 v102, v21, v21
	v_pk_add_f32 v[106:107], v[102:103], v[106:107] op_sel_hi:[0,1]
	v_lshlrev_b32_e32 v102, 16, v103
	v_mul_f32_e32 v55, 0xbfb8aa3b, v102
	v_exp_f32_e32 v55, v55
	v_and_b32_e32 v103, 0xffff0000, v103
	v_pk_mul_f32 v[22:23], v[22:23], v[102:103]
	v_add_f32_e32 v55, 1.0, v55
	v_rcp_f32_e32 v108, v55
	v_mul_f32_e32 v55, 0xbfb8aa3b, v103
	v_exp_f32_e32 v55, v55
	s_nop 0
	v_add_f32_e32 v55, 1.0, v55
	v_rcp_f32_e32 v109, v55
	s_nop 0
	v_pk_mul_f32 v[22:23], v[22:23], v[108:109]
	s_nop 0
	v_pk_fma_f32 v[102:103], v[22:23], v[22:23], v[106:107]
	s_waitcnt vmcnt(5)
	v_lshlrev_b32_e32 v106, 16, v98
	v_mul_f32_e32 v55, 0xbfb8aa3b, v106
	v_exp_f32_e32 v55, v55
	v_and_b32_e32 v107, 0xffff0000, v98
	v_mul_f32_e32 v104, v23, v23
	v_pk_add_f32 v[102:103], v[104:105], v[102:103] op_sel_hi:[0,1]
	v_add_f32_e32 v55, 1.0, v55
	v_rcp_f32_e32 v108, v55
	v_mul_f32_e32 v55, 0xbfb8aa3b, v107
	v_exp_f32_e32 v55, v55
	s_waitcnt lgkmcnt(2)
	v_lshlrev_b32_e32 v104, 16, v100
	v_and_b32_e32 v105, 0xffff0000, v100
	v_pk_fma_f32 v[16:17], v[70:71], v[104:105], v[16:17]
	v_add_f32_e32 v55, 1.0, v55
	v_rcp_f32_e32 v109, v55
	v_pk_mul_f32 v[16:17], v[16:17], v[106:107]
	v_lshlrev_b32_e32 v100, 16, v101
	v_and_b32_e32 v101, 0xffff0000, v101
	v_pk_mul_f32 v[16:17], v[16:17], v[108:109]
	v_pk_fma_f32 v[18:19], v[70:71], v[100:101], v[18:19]
	v_pk_fma_f32 v[102:103], v[16:17], v[16:17], v[102:103]
	v_mul_f32_e32 v98, v17, v17
	v_pk_add_f32 v[102:103], v[98:99], v[102:103] op_sel_hi:[0,1]
	v_lshlrev_b32_e32 v98, 16, v99
	v_mul_f32_e32 v55, 0xbfb8aa3b, v98
	v_exp_f32_e32 v55, v55
	v_and_b32_e32 v99, 0xffff0000, v99
	v_pk_mul_f32 v[18:19], v[18:19], v[98:99]
	v_add_f32_e32 v55, 1.0, v55
	v_rcp_f32_e32 v104, v55
	v_mul_f32_e32 v55, 0xbfb8aa3b, v99
	v_exp_f32_e32 v55, v55
	s_nop 0
	v_add_f32_e32 v55, 1.0, v55
	v_rcp_f32_e32 v105, v55
	s_nop 0
	v_pk_mul_f32 v[18:19], v[18:19], v[104:105]
	s_nop 0
	v_pk_fma_f32 v[98:99], v[18:19], v[18:19], v[102:103]
	s_waitcnt vmcnt(4)
	v_lshlrev_b32_e32 v102, 16, v94
	v_mul_f32_e32 v55, 0xbfb8aa3b, v102
	v_exp_f32_e32 v55, v55
	v_and_b32_e32 v103, 0xffff0000, v94
	v_mul_f32_e32 v100, v19, v19
	v_pk_add_f32 v[98:99], v[100:101], v[98:99] op_sel_hi:[0,1]
	v_add_f32_e32 v55, 1.0, v55
	v_rcp_f32_e32 v104, v55
	v_mul_f32_e32 v55, 0xbfb8aa3b, v103
	v_exp_f32_e32 v55, v55
	s_waitcnt lgkmcnt(1)
	v_lshlrev_b32_e32 v100, 16, v96
	v_and_b32_e32 v101, 0xffff0000, v96
	v_pk_fma_f32 v[24:25], v[70:71], v[100:101], v[24:25]
	v_add_f32_e32 v55, 1.0, v55
	v_rcp_f32_e32 v105, v55
	v_pk_mul_f32 v[24:25], v[24:25], v[102:103]
	v_lshlrev_b32_e32 v96, 16, v97
	v_and_b32_e32 v97, 0xffff0000, v97
	v_pk_mul_f32 v[24:25], v[24:25], v[104:105]
	v_pk_fma_f32 v[26:27], v[70:71], v[96:97], v[26:27]
	v_pk_fma_f32 v[98:99], v[24:25], v[24:25], v[98:99]
	v_mul_f32_e32 v94, v25, v25
	v_pk_add_f32 v[98:99], v[94:95], v[98:99] op_sel_hi:[0,1]
	v_lshlrev_b32_e32 v94, 16, v95
	v_mul_f32_e32 v55, 0xbfb8aa3b, v94
	v_exp_f32_e32 v55, v55
	v_and_b32_e32 v95, 0xffff0000, v95
	v_pk_mul_f32 v[26:27], v[26:27], v[94:95]
	v_add_f32_e32 v55, 1.0, v55
	v_rcp_f32_e32 v100, v55
	v_mul_f32_e32 v55, 0xbfb8aa3b, v95
	v_exp_f32_e32 v55, v55
	s_nop 0
	v_add_f32_e32 v55, 1.0, v55
	v_rcp_f32_e32 v101, v55
	s_nop 0
	v_pk_mul_f32 v[26:27], v[26:27], v[100:101]
	s_nop 0
	v_pk_fma_f32 v[94:95], v[26:27], v[26:27], v[98:99]
	v_mul_f32_e32 v96, v27, v27
	v_pk_add_f32 v[94:95], v[96:97], v[94:95] op_sel_hi:[0,1]
	v_mov_b32_e32 v55, v94
	s_nop 1
	v_permlane16_swap_b32_e32 v94, v55
	v_add_f32_e32 v55, v94, v55
	v_mov_b32_e32 v75, v55
	s_nop 1
	v_permlane32_swap_b32_e32 v55, v75
	s_and_saveexec_b64 s[0:1], s[42:43]
	v_readlane_b32 s72, v254, 1
	v_readlane_b32 s70, v254, 2
	v_readlane_b32 s71, v254, 3
	v_readlane_b32 s73, v254, 4
	s_mov_b32 s75, 0x8000
	s_mov_b32 s78, 0x200000
	s_mov_b32 s79, 0x7ffff
	v_add_f32_e32 v55, v55, v75
	ds_write_b32 v32, v55 offset:128
	s_or_b64 exec, exec, s[0:1]
	s_waitcnt vmcnt(3)
	v_lshlrev_b32_e32 v96, 16, v90
	v_mul_f32_e32 v55, 0xbfb8aa3b, v96
	v_exp_f32_e32 v55, v55
	v_and_b32_e32 v97, 0xffff0000, v90
	v_lshlrev_b32_e32 v90, 16, v91
	s_waitcnt lgkmcnt(0)
	v_lshlrev_b32_e32 v94, 16, v92
	v_add_f32_e32 v55, 1.0, v55
	v_rcp_f32_e32 v98, v55
	v_mul_f32_e32 v55, 0xbfb8aa3b, v97
	v_exp_f32_e32 v55, v55
	v_and_b32_e32 v95, 0xffff0000, v92
	v_pk_fma_f32 v[12:13], v[70:71], v[94:95], v[12:13]
	v_and_b32_e32 v91, 0xffff0000, v91
	v_add_f32_e32 v55, 1.0, v55
	v_rcp_f32_e32 v99, v55
	v_mul_f32_e32 v55, 0xbfb8aa3b, v90
	v_exp_f32_e32 v55, v55
	v_pk_mul_f32 v[12:13], v[12:13], v[96:97]
	v_lshlrev_b32_e32 v92, 16, v93
	v_and_b32_e32 v93, 0xffff0000, v93
	v_add_f32_e32 v55, 1.0, v55
	v_rcp_f32_e32 v96, v55
	v_mul_f32_e32 v55, 0xbfb8aa3b, v91
	v_exp_f32_e32 v55, v55
	v_pk_mul_f32 v[94:95], v[12:13], v[98:99]
	v_pk_fma_f32 v[14:15], v[70:71], v[92:93], v[14:15]
	v_mul_f32_e32 v12, v95, v95
	v_add_f32_e32 v55, 1.0, v55
	v_rcp_f32_e32 v97, v55
	v_pk_mul_f32 v[14:15], v[14:15], v[90:91]
	v_pk_fma_f32 v[12:13], v[94:95], v[94:95], v[12:13] op_sel_hi:[1,1,0]
	s_waitcnt vmcnt(2)
	v_lshlrev_b32_e32 v92, 16, v86
	v_pk_mul_f32 v[90:91], v[14:15], v[96:97]
	v_and_b32_e32 v93, 0xffff0000, v86
	v_pk_fma_f32 v[12:13], v[90:91], v[90:91], v[12:13]
	v_mul_f32_e32 v14, v91, v91
	v_pk_add_f32 v[12:13], v[14:15], v[12:13] op_sel_hi:[0,1]
	v_lshlrev_b32_e32 v14, 16, v88
	v_and_b32_e32 v15, 0xffff0000, v88
	v_mul_f32_e32 v55, 0xbfb8aa3b, v92
	v_pk_fma_f32 v[4:5], v[70:71], v[14:15], v[4:5]
	v_mul_f32_e32 v14, 0xbfb8aa3b, v93
	v_exp_f32_e32 v55, v55
	v_exp_f32_e32 v14, v14
	v_pk_mul_f32 v[4:5], v[4:5], v[92:93]
	v_and_b32_e32 v15, 0xffff0000, v87
	v_add_f32_e32 v55, 1.0, v55
	v_add_f32_e32 v14, 1.0, v14
	v_rcp_f32_e32 v96, v55
	v_rcp_f32_e32 v97, v14
	v_lshlrev_b32_e32 v14, 16, v87
	v_mul_f32_e32 v55, 0xbfb8aa3b, v14
	v_exp_f32_e32 v55, v55
	v_pk_mul_f32 v[92:93], v[4:5], v[96:97]
	v_add_f32_e32 v55, 1.0, v55
	v_pk_fma_f32 v[4:5], v[92:93], v[92:93], v[12:13]
	v_mul_f32_e32 v12, v93, v93
	v_pk_add_f32 v[4:5], v[12:13], v[4:5] op_sel_hi:[0,1]
	v_lshlrev_b32_e32 v12, 16, v89
	v_and_b32_e32 v13, 0xffff0000, v89
	v_pk_fma_f32 v[6:7], v[70:71], v[12:13], v[6:7]
	v_mul_f32_e32 v12, 0xbfb8aa3b, v15
	v_exp_f32_e32 v12, v12
	v_rcp_f32_e32 v86, v55
	v_pk_mul_f32 v[6:7], v[6:7], v[14:15]
	s_waitcnt vmcnt(1)
	v_and_b32_e32 v13, 0xffff0000, v82
	v_add_f32_e32 v12, 1.0, v12
	v_rcp_f32_e32 v87, v12
	v_lshlrev_b32_e32 v12, 16, v82
	v_mul_f32_e32 v14, 0xbfb8aa3b, v12
	v_exp_f32_e32 v14, v14
	v_pk_mul_f32 v[86:87], v[6:7], v[86:87]
	v_add_f32_e32 v14, 1.0, v14
	v_pk_fma_f32 v[4:5], v[86:87], v[86:87], v[4:5]
	v_mul_f32_e32 v6, v87, v87
	v_pk_add_f32 v[4:5], v[6:7], v[4:5] op_sel_hi:[0,1]
	v_lshlrev_b32_e32 v6, 16, v84
	v_and_b32_e32 v7, 0xffff0000, v84
	v_pk_fma_f32 v[0:1], v[70:71], v[6:7], v[0:1]
	v_mul_f32_e32 v6, 0xbfb8aa3b, v13
	v_exp_f32_e32 v6, v6
	v_rcp_f32_e32 v14, v14
	v_pk_mul_f32 v[0:1], v[0:1], v[12:13]
	v_and_b32_e32 v7, 0xffff0000, v83
	v_add_f32_e32 v6, 1.0, v6
	v_rcp_f32_e32 v15, v6
	v_lshlrev_b32_e32 v6, 16, v83
	v_mul_f32_e32 v12, 0xbfb8aa3b, v6
	v_exp_f32_e32 v12, v12
	v_pk_mul_f32 v[88:89], v[0:1], v[14:15]
	v_add_f32_e32 v12, 1.0, v12
	v_pk_fma_f32 v[0:1], v[88:89], v[88:89], v[4:5]
	v_mul_f32_e32 v4, v89, v89
	v_pk_add_f32 v[0:1], v[4:5], v[0:1] op_sel_hi:[0,1]
	v_lshlrev_b32_e32 v4, 16, v85
	v_and_b32_e32 v5, 0xffff0000, v85
	v_pk_fma_f32 v[2:3], v[70:71], v[4:5], v[2:3]
	v_mul_f32_e32 v4, 0xbfb8aa3b, v7
	v_exp_f32_e32 v4, v4
	v_rcp_f32_e32 v12, v12
	v_pk_mul_f32 v[2:3], v[2:3], v[6:7]
	s_waitcnt vmcnt(0)
	v_and_b32_e32 v5, 0xffff0000, v78
	v_add_f32_e32 v4, 1.0, v4
	v_rcp_f32_e32 v13, v4
	v_lshlrev_b32_e32 v4, 16, v78
	v_mul_f32_e32 v6, 0xbfb8aa3b, v4
	v_exp_f32_e32 v6, v6
	v_pk_mul_f32 v[82:83], v[2:3], v[12:13]
	v_add_f32_e32 v6, 1.0, v6
	v_pk_fma_f32 v[0:1], v[82:83], v[82:83], v[0:1]
	v_mul_f32_e32 v2, v83, v83
	v_pk_add_f32 v[0:1], v[2:3], v[0:1] op_sel_hi:[0,1]
	v_lshlrev_b32_e32 v2, 16, v80
	v_and_b32_e32 v3, 0xffff0000, v80
	v_pk_fma_f32 v[2:3], v[70:71], v[2:3], v[8:9]
	v_rcp_f32_e32 v6, v6
	v_pk_mul_f32 v[2:3], v[2:3], v[4:5]
	v_mul_f32_e32 v4, 0xbfb8aa3b, v5
	v_exp_f32_e32 v4, v4
	v_and_b32_e32 v5, 0xffff0000, v79
	v_add_f32_e32 v4, 1.0, v4
	v_rcp_f32_e32 v7, v4
	v_lshlrev_b32_e32 v4, 16, v79
	v_pk_mul_f32 v[84:85], v[2:3], v[6:7]
	s_nop 0
	v_pk_fma_f32 v[0:1], v[84:85], v[84:85], v[0:1]
	v_mul_f32_e32 v2, v85, v85
	v_pk_add_f32 v[0:1], v[2:3], v[0:1] op_sel_hi:[0,1]
	v_lshlrev_b32_e32 v2, 16, v81
	v_and_b32_e32 v3, 0xffff0000, v81
	v_pk_fma_f32 v[2:3], v[70:71], v[2:3], v[10:11]
	v_mul_f32_e32 v6, 0xbfb8aa3b, v4
	v_pk_mul_f32 v[2:3], v[2:3], v[4:5]
	v_mul_f32_e32 v4, 0xbfb8aa3b, v5
	v_exp_f32_e32 v6, v6
	v_exp_f32_e32 v4, v4
	v_add_f32_e32 v6, 1.0, v6
	v_add_f32_e32 v4, 1.0, v4
	v_rcp_f32_e32 v6, v6
	v_rcp_f32_e32 v7, v4
	s_nop 0
	v_pk_mul_f32 v[70:71], v[2:3], v[6:7]
	s_nop 0
	v_pk_fma_f32 v[0:1], v[70:71], v[70:71], v[0:1]
	v_mul_f32_e32 v2, v71, v71
	v_pk_add_f32 v[0:1], v[2:3], v[0:1] op_sel_hi:[0,1]
	v_mov_b32_e32 v1, v0
	s_nop 1
	v_permlane16_swap_b32_e32 v0, v1
	v_add_f32_e32 v0, v0, v1
	v_mov_b32_e32 v1, v0
	s_nop 1
	v_permlane32_swap_b32_e32 v0, v1
	s_and_saveexec_b64 s[0:1], s[42:43]
	s_cbranch_execz .LBB0_1267
	v_add_f32_e32 v0, v0, v1
	ds_write_b32 v32, v0 offset:192
	s_branch .LBB0_1267
